# accumulator zeroing between tiles with 64 v_mov_b64 instead of 128 v_mov_b32 (all five GEMM phases), on top of the wait-placement / load-batching / converter edits
# speedup vs baseline: 1.0031x; 1.0031x over previous
.LBB0_315:
	s_andn2_b64 vcc, exec, s[2:3]
	s_cbranch_vccnz .LBB0_477
	s_add_u32 s12, s92, 0x28ee1c00
	s_addc_u32 s2, s93, 0
	s_add_u32 s16, s92, 0x3e0400
	s_addc_u32 s3, s93, 0
	s_lshl_b32 s4, s86, 10
	s_waitcnt vmcnt(9)
	v_lshlrev_b32_e32 v24, 4, v144
	v_or_b32_e32 v0, s4, v24
	v_ashrrev_i32_e32 v1, 31, v0
	v_lshrrev_b32_e32 v1, 22, v1
	v_add_u32_e32 v1, v0, v1
	v_ashrrev_i32_e32 v1, 10, v1
	v_mul_i32_i24_e32 v2, 0x400, v1
	v_sub_u32_e32 v2, v0, v2
	v_lshrrev_b32_e32 v3, 4, v2
	v_bitop3_b32 v2, v3, v2, 32 bitop3:0x6c
	s_waitcnt vmcnt(8)
	v_ashrrev_i32_e32 v4, 31, v2
	v_lshrrev_b32_e32 v4, 26, v4
	v_lshlrev_b32_e32 v3, 3, v1
	v_add_u32_e32 v4, v2, v4
	v_and_b32_e32 v3, -16, v3
	v_ashrrev_i32_e32 v5, 6, v4
	v_add_u32_e32 v25, v5, v3
	v_and_b32_e32 v3, 0xc0, v4
	v_lshlrev_b32_e32 v1, 5, v1
	v_sub_u32_e32 v2, v2, v3
	v_mov_b32_e32 v3, 1
	v_and_b32_e32 v1, 32, v1
	v_ashrrev_i16_sdwa v2, v3, sext(v2) dst_sel:DWORD dst_unused:UNUSED_PAD src0_sel:DWORD src1_sel:BYTE_0
	v_add_u32_sdwa v26, v1, sext(v2) dst_sel:DWORD dst_unused:UNUSED_PAD src0_sel:DWORD src1_sel:WORD_0
	v_lshlrev_b32_e32 v1, 1, v25
	v_lshrrev_b32_e32 v2, 2, v25
	v_and_b32_e32 v4, 3, v5
	s_mov_b32 s5, 0xfffe0
	v_and_b32_e32 v1, 24, v1
	v_and_b32_e32 v2, 4, v2
	v_and_or_b32 v4, v25, s5, v4
	v_or3_b32 v1, v4, v2, v1
	v_lshlrev_b32_e32 v27, 1, v26
	v_add_u32_e32 v0, 0x2000, v0
	v_lshl_add_u32 v154, v1, 12, v27
	v_ashrrev_i32_e32 v1, 31, v0
	v_lshrrev_b32_e32 v1, 22, v1
	v_add_u32_e32 v1, v0, v1
	v_ashrrev_i32_e32 v1, 10, v1
	v_mul_i32_i24_e32 v2, 0x400, v1
	v_sub_u32_e32 v0, v0, v2
	v_lshrrev_b32_e32 v2, 4, v0
	v_bitop3_b32 v0, v2, v0, 32 bitop3:0x6c
	v_ashrrev_i32_e32 v4, 31, v0
	v_lshrrev_b32_e32 v4, 26, v4
	v_lshlrev_b32_e32 v2, 3, v1
	v_add_u32_e32 v4, v0, v4
	v_and_b32_e32 v2, -16, v2
	v_ashrrev_i32_e32 v5, 6, v4
	s_waitcnt vmcnt(7)
	v_add_u32_e32 v28, v5, v2
	v_and_b32_e32 v2, 0xffc0, v4
	v_sub_u32_e32 v0, v0, v2
	v_lshrrev_b16_e32 v2, 7, v0
	v_and_b32_e32 v2, 1, v2
	v_lshlrev_b32_e32 v1, 5, v1
	v_add_u16_e32 v0, v0, v2
	v_and_b32_e32 v1, 32, v1
	v_ashrrev_i16_sdwa v0, v3, sext(v0) dst_sel:DWORD dst_unused:UNUSED_PAD src0_sel:DWORD src1_sel:BYTE_0
	v_add_u32_sdwa v29, v1, sext(v0) dst_sel:DWORD dst_unused:UNUSED_PAD src0_sel:DWORD src1_sel:WORD_0
	v_lshlrev_b32_e32 v0, 1, v28
	v_lshrrev_b32_e32 v1, 2, v28
	v_and_b32_e32 v2, 3, v5
	s_add_i32 s34, s4, 0
	v_and_b32_e32 v0, 24, v0
	v_and_b32_e32 v1, 4, v1
	v_and_or_b32 v2, v28, s5, v2
	s_mov_b32 s15, 0x20000
	s_mov_b32 s14, -1
	s_add_i32 s35, s34, 0x10000
	v_or3_b32 v0, v2, v1, v0
	v_lshlrev_b32_e32 v30, 1, v29
	s_and_b32 s17, s3, 0xffff
	s_mov_b32 s18, s14
	s_mov_b32 s19, s15
	s_lshl_b32 s7, s30, 20
	s_mov_b32 m0, s35
	s_add_i32 s36, s34, 0x12000
	v_lshl_add_u32 v155, v0, 12, v30
	v_mov_b64 v[136:137], 0
	v_mov_b64 v[138:139], 0
	v_mov_b64 v[140:141], 0
	v_mov_b64 v[142:143], 0
	v_mov_b64 v[124:125], 0
	v_mov_b64 v[126:127], 0
	v_mov_b64 v[120:121], 0
	v_mov_b64 v[122:123], 0
	v_mov_b64 v[108:109], 0
	v_mov_b64 v[110:111], 0
	v_mov_b64 v[104:105], 0
	v_mov_b64 v[106:107], 0
	v_mov_b64 v[92:93], 0
	v_mov_b64 v[94:95], 0
	v_mov_b64 v[88:89], 0
	v_mov_b64 v[90:91], 0
	v_mov_b64 v[132:133], 0
	v_mov_b64 v[134:135], 0
	v_mov_b64 v[128:129], 0
	v_mov_b64 v[130:131], 0
	v_mov_b64 v[116:117], 0
	v_mov_b64 v[118:119], 0
	v_mov_b64 v[112:113], 0
	v_mov_b64 v[114:115], 0
	v_mov_b64 v[100:101], 0
	v_mov_b64 v[102:103], 0
	v_mov_b64 v[96:97], 0
	v_mov_b64 v[98:99], 0
	v_mov_b64 v[84:85], 0
	v_mov_b64 v[86:87], 0
	v_mov_b64 v[80:81], 0
	v_mov_b64 v[82:83], 0
	v_mov_b64 v[76:77], 0
	v_mov_b64 v[78:79], 0
	v_mov_b64 v[72:73], 0
	v_mov_b64 v[74:75], 0
	v_mov_b64 v[60:61], 0
	v_mov_b64 v[62:63], 0
	s_waitcnt vmcnt(4)
	v_mov_b64 v[56:57], 0
	v_mov_b64 v[58:59], 0
	v_mov_b64 v[36:37], 0
	v_mov_b64 v[38:39], 0
	v_mov_b64 v[32:33], 0
	v_mov_b64 v[34:35], 0
	v_mov_b64 v[12:13], 0
	v_mov_b64 v[14:15], 0
	v_mov_b64 v[8:9], 0
	v_mov_b64 v[10:11], 0
	v_mov_b64 v[68:69], 0
	v_mov_b64 v[70:71], 0
	v_mov_b64 v[64:65], 0
	v_mov_b64 v[66:67], 0
	v_mov_b64 v[52:53], 0
	v_mov_b64 v[54:55], 0
	v_mov_b64 v[48:49], 0
	v_mov_b64 v[50:51], 0
	v_mov_b64 v[20:21], 0
	v_mov_b64 v[22:23], 0
	v_mov_b64 v[16:17], 0
	v_mov_b64 v[18:19], 0
	v_mov_b64 v[4:5], 0
	v_mov_b64 v[6:7], 0
	v_mov_b64 v[0:1], 0
	v_mov_b64 v[2:3], 0
	buffer_load_dwordx4 v154, s[16:19], s7 offen lds
	s_mov_b32 m0, s36
	s_add_i32 s37, s34, 0x14000
	s_and_b32 s13, s2, 0xffff
	buffer_load_dwordx4 v155, s[16:19], s7 offen lds
	s_or_b32 s2, s7, 0x80000
	s_mov_b32 m0, s37
	s_add_i32 s38, s34, 0x16000
	buffer_load_dwordx4 v154, s[16:19], s2 offen lds
	s_mov_b32 m0, s38
	v_lshl_add_u32 v156, v25, 12, v27
	s_lshl_b32 s6, s33, 20
	buffer_load_dwordx4 v155, s[16:19], s2 offen lds
	s_mov_b32 m0, s34
	s_add_i32 s39, s34, 0x2000
	v_lshl_add_u32 v157, v28, 12, v30
	v_lshl_add_u32 v25, v25, 11, v26
	v_mov_b32_e32 v26, 0x80000
	buffer_load_dwordx4 v156, s[12:15], s6 offen lds
	s_mov_b32 m0, s39
	s_add_i32 s40, s34, 0x4000
	v_lshl_add_u32 v158, v25, 1, v26
	v_lshl_add_u32 v25, v28, 11, v29
	buffer_load_dwordx4 v157, s[12:15], s6 offen lds
	s_mov_b32 m0, s40
	s_add_i32 s41, s34, 0x6000
	v_lshl_add_u32 v159, v25, 1, v26
	buffer_load_dwordx4 v158, s[12:15], s6 offen lds
	s_mov_b32 m0, s41
	s_lshr_b32 s2, s90, 8
	buffer_load_dwordx4 v159, s[12:15], s6 offen lds
	s_cmp_eq_u32 s2, 1
	s_cselect_b64 s[10:11], -1, 0
	s_cmp_lg_u32 s2, 1
	s_mov_b32 s42, 0
	s_cbranch_scc1 .LBB0_318
	s_barrier

.LBB0_473:
	s_nop 0
	v_cvt_pk_bf16_f32 v0, v14, v15
	v_cvt_pk_bf16_f32 v1, v18, v19
	v_cvt_pk_bf16_f32 v2, v12, v13
	v_cvt_pk_bf16_f32 v3, v16, v17
	s_and_b64 vcc, exec, s[2:3]
	s_mov_b64 s[2:3], -1
	global_store_dwordx4 v[10:11], v[0:3], off offset:256
	s_cbranch_vccnz .LBB0_320
	s_andn2_b64 vcc, exec, s[10:11]
	v_mov_b64 v[136:137], 0
	v_mov_b64 v[138:139], 0
	v_mov_b64 v[140:141], 0
	v_mov_b64 v[142:143], 0
	v_mov_b64 v[124:125], 0
	v_mov_b64 v[126:127], 0
	v_mov_b64 v[120:121], 0
	v_mov_b64 v[122:123], 0
	v_mov_b64 v[108:109], 0
	v_mov_b64 v[110:111], 0
	v_mov_b64 v[104:105], 0
	v_mov_b64 v[106:107], 0
	v_mov_b64 v[92:93], 0
	v_mov_b64 v[94:95], 0
	v_mov_b64 v[88:89], 0
	v_mov_b64 v[90:91], 0
	v_mov_b64 v[132:133], 0
	v_mov_b64 v[134:135], 0
	v_mov_b64 v[128:129], 0
	v_mov_b64 v[130:131], 0
	v_mov_b64 v[116:117], 0
	v_mov_b64 v[118:119], 0
	v_mov_b64 v[112:113], 0
	v_mov_b64 v[114:115], 0
	v_mov_b64 v[100:101], 0
	v_mov_b64 v[102:103], 0
	v_mov_b64 v[96:97], 0
	v_mov_b64 v[98:99], 0
	v_mov_b64 v[84:85], 0
	v_mov_b64 v[86:87], 0
	v_mov_b64 v[80:81], 0
	v_mov_b64 v[82:83], 0
	v_mov_b64 v[76:77], 0
	v_mov_b64 v[78:79], 0
	v_mov_b64 v[72:73], 0
	v_mov_b64 v[74:75], 0
	v_mov_b64 v[60:61], 0
	v_mov_b64 v[62:63], 0
	v_mov_b64 v[56:57], 0
	v_mov_b64 v[58:59], 0
	v_mov_b64 v[36:37], 0
	v_mov_b64 v[38:39], 0
	v_mov_b64 v[32:33], 0
	v_mov_b64 v[34:35], 0
	v_mov_b64 v[12:13], 0
	v_mov_b64 v[14:15], 0
	v_mov_b64 v[8:9], 0
	v_mov_b64 v[10:11], 0
	v_mov_b64 v[68:69], 0
	v_mov_b64 v[70:71], 0
	v_mov_b64 v[64:65], 0
	v_mov_b64 v[66:67], 0
	v_mov_b64 v[52:53], 0
	v_mov_b64 v[54:55], 0
	v_mov_b64 v[48:49], 0
	v_mov_b64 v[50:51], 0
	v_mov_b64 v[20:21], 0
	v_mov_b64 v[22:23], 0
	v_mov_b64 v[16:17], 0
	v_mov_b64 v[18:19], 0
	v_mov_b64 v[4:5], 0
	v_mov_b64 v[6:7], 0
	v_mov_b64 v[0:1], 0
	v_mov_b64 v[2:3], 0
	s_cbranch_vccnz .LBB0_319
	s_barrier
	s_branch .LBB0_319

.LBB0_856:
	s_ashr_i32 s4, s7, 3
	s_add_u32 s8, s92, 0x30ee1c00
	s_addc_u32 s5, s93, 0
	v_mbcnt_lo_u32_b32 v0, -1, 0
	s_add_u32 s12, s92, 0x24e0400
	v_mbcnt_hi_u32_b32 v128, -1, v0
	s_addc_u32 s7, s93, 0
	s_lshl_b32 s16, s86, 10
	v_lshl_or_b32 v0, v128, 4, s16
	v_ashrrev_i32_e32 v1, 31, v0
	v_lshrrev_b32_e32 v1, 22, v1
	v_add_u32_e32 v1, v0, v1
	v_ashrrev_i32_e32 v1, 10, v1
	v_mul_i32_i24_e32 v2, 0x400, v1
	v_sub_u32_e32 v2, v0, v2
	v_lshrrev_b32_e32 v3, 4, v2
	v_bitop3_b32 v2, v3, v2, 32 bitop3:0x6c
	s_waitcnt vmcnt(8)
	v_ashrrev_i32_e32 v4, 31, v2
	v_lshrrev_b32_e32 v4, 26, v4
	v_lshlrev_b32_e32 v3, 3, v1
	v_add_u32_e32 v4, v2, v4
	v_and_b32_e32 v3, -16, v3
	v_ashrrev_i32_e32 v5, 6, v4
	v_add_u32_e32 v129, v5, v3
	v_and_b32_e32 v3, 0xc0, v4
	v_lshlrev_b32_e32 v1, 5, v1
	v_sub_u32_e32 v2, v2, v3
	v_mov_b32_e32 v3, 1
	v_and_b32_e32 v1, 32, v1
	v_ashrrev_i16_sdwa v2, v3, sext(v2) dst_sel:DWORD dst_unused:UNUSED_PAD src0_sel:DWORD src1_sel:BYTE_0
	v_add_u32_sdwa v130, v1, sext(v2) dst_sel:DWORD dst_unused:UNUSED_PAD src0_sel:DWORD src1_sel:WORD_0
	v_lshlrev_b32_e32 v1, 1, v129
	v_lshrrev_b32_e32 v2, 2, v129
	v_and_b32_e32 v4, 3, v5
	s_mov_b32 s9, 0x1fffe0
	v_and_b32_e32 v1, 24, v1
	v_and_b32_e32 v2, 4, v2
	v_and_or_b32 v4, v129, s9, v4
	v_or3_b32 v1, v4, v2, v1
	v_lshlrev_b32_e32 v131, 1, v130
	v_add_u32_e32 v0, 0x2000, v0
	v_lshl_add_u32 v194, v1, 11, v131
	v_ashrrev_i32_e32 v1, 31, v0
	v_lshrrev_b32_e32 v1, 22, v1
	v_add_u32_e32 v1, v0, v1
	v_ashrrev_i32_e32 v1, 10, v1
	v_mul_i32_i24_e32 v2, 0x400, v1
	v_sub_u32_e32 v0, v0, v2
	v_lshrrev_b32_e32 v2, 4, v0
	v_bitop3_b32 v0, v2, v0, 32 bitop3:0x6c
	v_ashrrev_i32_e32 v4, 31, v0
	v_lshrrev_b32_e32 v4, 26, v4
	v_lshlrev_b32_e32 v2, 3, v1
	v_add_u32_e32 v4, v0, v4
	v_and_b32_e32 v2, -16, v2
	v_ashrrev_i32_e32 v5, 6, v4
	v_add_u32_e32 v132, v5, v2
	v_and_b32_e32 v2, 0xffc0, v4
	v_sub_u32_e32 v0, v0, v2
	v_lshrrev_b16_e32 v2, 7, v0
	v_and_b32_e32 v2, 1, v2
	v_add_u16_e32 v0, v0, v2
	v_and_b32_e32 v2, 3, v5
	s_add_i32 s4, s6, s4
	v_and_or_b32 v2, v132, s9, v2
	s_and_b32 s9, s5, 0xffff
	s_ashr_i32 s5, s4, 31
	s_lshr_b32 s5, s5, 27
	s_add_i32 s5, s4, s5
	s_ashr_i32 s6, s5, 5
	s_andn2_b32 s5, s5, 31
	s_sub_i32 s4, s4, s5
	s_bfe_i32 s5, s4, 0x80000
	s_bfe_u32 s5, s5, 0x2000d
	v_lshlrev_b32_e32 v1, 5, v1
	s_add_i32 s5, s4, s5
	v_and_b32_e32 v1, 32, v1
	v_ashrrev_i16_sdwa v0, v3, sext(v0) dst_sel:DWORD dst_unused:UNUSED_PAD src0_sel:DWORD src1_sel:BYTE_0
	s_and_b32 s13, s7, 0xffff
	s_bfe_i32 s7, s5, 0x80000
	v_add_u32_sdwa v133, v1, sext(v0) dst_sel:DWORD dst_unused:UNUSED_PAD src0_sel:DWORD src1_sel:WORD_0
	v_lshlrev_b32_e32 v0, 1, v132
	v_lshrrev_b32_e32 v1, 2, v132
	s_sext_i32_i16 s7, s7
	s_add_i32 s26, s16, 0
	s_mov_b32 s10, -1
	v_and_b32_e32 v0, 24, v0
	v_and_b32_e32 v1, 4, v1
	s_mov_b32 s11, 0x20000
	s_and_b32 s5, s5, 0xfc
	s_ashr_i32 s51, s7, 2
	s_add_i32 s27, s26, 0x10000
	v_or3_b32 v0, v2, v1, v0
	v_lshlrev_b32_e32 v134, 1, v133
	s_mov_b32 s14, s10
	s_mov_b32 s15, s11
	s_sub_i32 s4, s4, s5
	s_lshl_b32 s50, s51, 19
	s_mov_b32 m0, s27
	s_add_i32 s28, s26, 0x12000
	v_lshl_add_u32 v195, v0, 11, v134
	s_lshl_b32 s6, s6, 2
	s_sext_i32_i8 s4, s4
	v_mov_b64 v[124:125], 0
	v_mov_b64 v[126:127], 0
	v_mov_b64 v[120:121], 0
	v_mov_b64 v[122:123], 0
	v_mov_b64 v[108:109], 0
	v_mov_b64 v[110:111], 0
	v_mov_b64 v[104:105], 0
	v_mov_b64 v[106:107], 0
	v_mov_b64 v[92:93], 0
	v_mov_b64 v[94:95], 0
	v_mov_b64 v[88:89], 0
	v_mov_b64 v[90:91], 0
	v_mov_b64 v[76:77], 0
	v_mov_b64 v[78:79], 0
	v_mov_b64 v[72:73], 0
	v_mov_b64 v[74:75], 0
	v_mov_b64 v[116:117], 0
	v_mov_b64 v[118:119], 0
	v_mov_b64 v[112:113], 0
	v_mov_b64 v[114:115], 0
	v_mov_b64 v[100:101], 0
	v_mov_b64 v[102:103], 0
	v_mov_b64 v[96:97], 0
	v_mov_b64 v[98:99], 0
	v_mov_b64 v[84:85], 0
	v_mov_b64 v[86:87], 0
	v_mov_b64 v[80:81], 0
	v_mov_b64 v[82:83], 0
	v_mov_b64 v[68:69], 0
	v_mov_b64 v[70:71], 0
	v_mov_b64 v[64:65], 0
	v_mov_b64 v[66:67], 0
	s_waitcnt vmcnt(7)
	v_mov_b64 v[60:61], 0
	v_mov_b64 v[62:63], 0
	s_waitcnt vmcnt(4)
	v_mov_b64 v[56:57], 0
	v_mov_b64 v[58:59], 0
	v_mov_b64 v[44:45], 0
	v_mov_b64 v[46:47], 0
	v_mov_b64 v[40:41], 0
	v_mov_b64 v[42:43], 0
	v_mov_b64 v[28:29], 0
	v_mov_b64 v[30:31], 0
	v_mov_b64 v[24:25], 0
	v_mov_b64 v[26:27], 0
	v_mov_b64 v[12:13], 0
	v_mov_b64 v[14:15], 0
	v_mov_b64 v[8:9], 0
	v_mov_b64 v[10:11], 0
	v_mov_b64 v[52:53], 0
	v_mov_b64 v[54:55], 0
	v_mov_b64 v[48:49], 0
	v_mov_b64 v[50:51], 0
	v_mov_b64 v[36:37], 0
	v_mov_b64 v[38:39], 0
	v_mov_b64 v[32:33], 0
	v_mov_b64 v[34:35], 0
	v_mov_b64 v[20:21], 0
	v_mov_b64 v[22:23], 0
	v_mov_b64 v[16:17], 0
	v_mov_b64 v[18:19], 0
	v_mov_b64 v[0:1], 0
	v_mov_b64 v[2:3], 0
	v_mov_b64 v[4:5], 0
	v_mov_b64 v[6:7], 0
	buffer_load_dwordx4 v194, s[12:15], s50 offen lds
	s_mov_b32 m0, s28
	s_add_i32 s29, s26, 0x14000
	s_add_i32 s52, s6, s4
	buffer_load_dwordx4 v195, s[12:15], s50 offen lds
	s_or_b32 s4, s50, 0x40000
	s_mov_b32 m0, s29
	s_add_i32 s30, s26, 0x16000
	buffer_load_dwordx4 v194, s[12:15], s4 offen lds
	s_mov_b32 m0, s30
	v_lshl_add_u32 v196, v129, 11, v131
	s_lshl_b32 s49, s52, 19
	buffer_load_dwordx4 v195, s[12:15], s4 offen lds
	s_mov_b32 m0, s26
	s_add_i32 s31, s26, 0x2000
	v_lshl_add_u32 v197, v132, 11, v134
	v_lshl_add_u32 v129, v129, 10, v130
	v_mov_b32_e32 v130, 0x40000
	buffer_load_dwordx4 v196, s[8:11], s49 offen lds
	s_mov_b32 m0, s31
	s_add_i32 s33, s26, 0x4000
	v_lshl_add_u32 v198, v129, 1, v130
	v_lshl_add_u32 v129, v132, 10, v133
	buffer_load_dwordx4 v197, s[8:11], s49 offen lds
	s_mov_b32 m0, s33
	s_add_i32 s34, s26, 0x6000
	v_lshl_add_u32 v199, v129, 1, v130
	buffer_load_dwordx4 v198, s[8:11], s49 offen lds
	s_mov_b32 m0, s34
	s_lshr_b32 s4, s90, 8
	buffer_load_dwordx4 v199, s[8:11], s49 offen lds
	s_cmp_eq_u32 s4, 1
	s_cselect_b64 s[6:7], -1, 0
	s_cmp_lg_u32 s4, 1
	s_mov_b32 s35, 0
	s_cbranch_scc1 .LBB0_858
	s_barrier

.LBB0_875:
	global_load_dwordx4 v[178:181], v[144:145], off
	global_load_dwordx4 v[182:185], v[144:145], off offset:256
	global_load_dwordx4 v[186:189], v[146:147], off
	s_nop 0
	global_load_dwordx4 v[144:147], v[146:147], off offset:256
	s_nop 0
	global_load_dwordx4 v[140:143], v[174:175], off
	global_load_dwordx4 v[136:139], v[174:175], off offset:256
	global_load_dwordx4 v[132:135], v[176:177], off
	global_load_dwordx4 v[128:131], v[176:177], off offset:256
	v_lshlrev_b64 v[172:173], 12, v[172:173]
	v_lshl_add_u64 v[172:173], s[16:17], 0, v[172:173]
	v_lshl_add_u64 v[172:173], v[172:173], 0, v[148:149]
	s_and_b64 vcc, exec, s[4:5]
	s_mov_b64 s[4:5], -1
	s_waitcnt vmcnt(7)
	v_lshlrev_b32_e32 v174, 16, v178
	v_and_b32_e32 v175, 0xffff0000, v178
	v_lshlrev_b32_e32 v176, 16, v179
	v_and_b32_e32 v177, 0xffff0000, v179
	v_lshlrev_b32_e32 v178, 16, v180
	v_and_b32_e32 v179, 0xffff0000, v180
	v_lshlrev_b32_e32 v180, 16, v181
	v_and_b32_e32 v181, 0xffff0000, v181
	v_mul_f32_e32 v181, 0xbfb8aa3b, v181
	v_mul_f32_e32 v174, 0xbfb8aa3b, v174
	v_mul_f32_e32 v175, 0xbfb8aa3b, v175
	v_mul_f32_e32 v176, 0xbfb8aa3b, v176
	v_mul_f32_e32 v177, 0xbfb8aa3b, v177
	v_mul_f32_e32 v178, 0xbfb8aa3b, v178
	v_mul_f32_e32 v179, 0xbfb8aa3b, v179
	v_mul_f32_e32 v180, 0xbfb8aa3b, v180
	v_exp_f32_e32 v181, v181
	v_exp_f32_e32 v174, v174
	v_exp_f32_e32 v175, v175
	v_exp_f32_e32 v176, v176
	v_exp_f32_e32 v177, v177
	v_exp_f32_e32 v178, v178
	v_exp_f32_e32 v179, v179
	v_exp_f32_e32 v180, v180
	v_add_f32_e32 v181, 1.0, v181
	v_add_f32_e32 v174, 1.0, v174
	v_add_f32_e32 v175, 1.0, v175
	v_add_f32_e32 v176, 1.0, v176
	v_add_f32_e32 v177, 1.0, v177
	v_add_f32_e32 v178, 1.0, v178
	v_add_f32_e32 v179, 1.0, v179
	v_add_f32_e32 v180, 1.0, v180
	v_rcp_f32_e32 v181, v181
	v_rcp_f32_e32 v174, v174
	v_rcp_f32_e32 v175, v175
	v_rcp_f32_e32 v176, v176
	v_rcp_f32_e32 v177, v177
	v_rcp_f32_e32 v178, v178
	v_rcp_f32_e32 v179, v179
	v_rcp_f32_e32 v180, v180
	v_max_f32_e32 v181, 0x35800000, v181
	s_waitcnt vmcnt(6)
	v_lshlrev_b32_e32 v190, 16, v182
	v_and_b32_e32 v182, 0xffff0000, v182
	v_max_f32_e32 v174, 0x35800000, v174
	v_max_f32_e32 v175, 0x35800000, v175
	v_max_f32_e32 v176, 0x35800000, v176
	v_max_f32_e32 v177, 0x35800000, v177
	v_max_f32_e32 v178, 0x35800000, v178
	v_max_f32_e32 v179, 0x35800000, v179
	v_max_f32_e32 v180, 0x35800000, v180
	v_mul_f32_e32 v123, v123, v181
	v_lshlrev_b32_e32 v191, 16, v183
	v_and_b32_e32 v183, 0xffff0000, v183
	v_lshlrev_b32_e32 v192, 16, v184
	v_and_b32_e32 v184, 0xffff0000, v184
	v_mul_f32_e32 v190, 0xbfb8aa3b, v190
	v_mul_f32_e32 v182, 0xbfb8aa3b, v182
	v_mul_f32_e32 v124, v124, v174
	v_mul_f32_e32 v125, v125, v175
	v_mul_f32_e32 v126, v126, v176
	v_mul_f32_e32 v127, v127, v177
	v_mul_f32_e32 v174, v120, v178
	v_mul_f32_e32 v175, v121, v179
	v_mul_f32_e32 v176, v122, v180
	v_cvt_pk_bf16_f32 v120, v124, v125
	v_cvt_pk_bf16_f32 v121, v126, v127
	v_cvt_pk_bf16_f32 v122, v174, v175
	v_cvt_pk_bf16_f32 v123, v176, v123
	v_lshlrev_b32_e32 v193, 16, v185
	v_and_b32_e32 v185, 0xffff0000, v185
	v_mul_f32_e32 v191, 0xbfb8aa3b, v191
	v_mul_f32_e32 v183, 0xbfb8aa3b, v183
	v_exp_f32_e32 v190, v190
	v_exp_f32_e32 v182, v182
	global_store_dwordx4 v[172:173], v[120:123], off
	v_mul_f32_e32 v124, 0xbfb8aa3b, v184
	v_exp_f32_e32 v191, v191
	v_mul_f32_e32 v123, 0xbfb8aa3b, v192
	v_exp_f32_e32 v183, v183
	v_exp_f32_e32 v123, v123
	v_exp_f32_e32 v124, v124
	v_mul_f32_e32 v125, 0xbfb8aa3b, v193
	v_mul_f32_e32 v126, 0xbfb8aa3b, v185
	v_exp_f32_e32 v125, v125
	v_exp_f32_e32 v126, v126
	v_add_f32_e32 v190, 1.0, v190
	v_add_f32_e32 v182, 1.0, v182
	v_add_f32_e32 v191, 1.0, v191
	v_rcp_f32_e32 v190, v190
	v_rcp_f32_e32 v182, v182
	v_add_f32_e32 v122, 1.0, v183
	v_add_f32_e32 v123, 1.0, v123
	v_add_f32_e32 v124, 1.0, v124
	v_rcp_f32_e32 v191, v191
	v_rcp_f32_e32 v122, v122
	v_rcp_f32_e32 v123, v123
	v_rcp_f32_e32 v124, v124
	v_add_f32_e32 v125, 1.0, v125
	v_add_f32_e32 v126, 1.0, v126
	v_rcp_f32_e32 v125, v125
	v_rcp_f32_e32 v126, v126
	v_max_f32_e32 v190, 0x35800000, v190
	v_max_f32_e32 v120, 0x35800000, v182
	v_max_f32_e32 v121, 0x35800000, v191
	v_max_f32_e32 v122, 0x35800000, v122
	v_max_f32_e32 v123, 0x35800000, v123
	v_max_f32_e32 v124, 0x35800000, v124
	v_mul_f32_e32 v116, v116, v190
	v_mul_f32_e32 v117, v117, v120
	v_max_f32_e32 v125, 0x35800000, v125
	v_max_f32_e32 v126, 0x35800000, v126
	v_cvt_pk_bf16_f32 v116, v116, v117
	v_mul_f32_e32 v117, v118, v121
	v_mul_f32_e32 v118, v119, v122
	v_mul_f32_e32 v112, v112, v123
	v_mul_f32_e32 v113, v113, v124
	v_cvt_pk_bf16_f32 v117, v117, v118
	v_cvt_pk_bf16_f32 v118, v112, v113
	v_mul_f32_e32 v112, v114, v125
	v_mul_f32_e32 v113, v115, v126
	v_cvt_pk_bf16_f32 v119, v112, v113
	s_waitcnt vmcnt(6)
	v_lshlrev_b32_e32 v114, 16, v186
	v_and_b32_e32 v115, 0xffff0000, v186
	global_store_dwordx4 v[172:173], v[116:119], off offset:256
	v_mul_f32_e32 v114, 0xbfb8aa3b, v114
	v_mul_f32_e32 v115, 0xbfb8aa3b, v115
	v_lshlrev_b32_e32 v116, 16, v187
	v_and_b32_e32 v117, 0xffff0000, v187
	v_lshlrev_b32_e32 v118, 16, v188
	v_and_b32_e32 v119, 0xffff0000, v188
	v_exp_f32_e32 v114, v114
	v_lshlrev_b32_e32 v120, 16, v189
	v_and_b32_e32 v121, 0xffff0000, v189
	v_exp_f32_e32 v115, v115
	v_mul_f32_e32 v116, 0xbfb8aa3b, v116
	v_mul_f32_e32 v117, 0xbfb8aa3b, v117
	v_mul_f32_e32 v118, 0xbfb8aa3b, v118
	v_mul_f32_e32 v119, 0xbfb8aa3b, v119
	v_exp_f32_e32 v116, v116
	v_exp_f32_e32 v117, v117
	v_exp_f32_e32 v118, v118
	v_exp_f32_e32 v119, v119
	v_mul_f32_e32 v120, 0xbfb8aa3b, v120
	v_mul_f32_e32 v121, 0xbfb8aa3b, v121
	v_exp_f32_e32 v120, v120
	v_exp_f32_e32 v121, v121
	v_add_f32_e32 v114, 1.0, v114
	v_add_f32_e32 v115, 1.0, v115
	v_rcp_f32_e32 v114, v114
	v_rcp_f32_e32 v115, v115
	v_add_f32_e32 v116, 1.0, v116
	v_add_f32_e32 v117, 1.0, v117
	v_add_f32_e32 v118, 1.0, v118
	v_add_f32_e32 v119, 1.0, v119
	v_rcp_f32_e32 v116, v116
	v_rcp_f32_e32 v117, v117
	v_rcp_f32_e32 v118, v118
	v_rcp_f32_e32 v119, v119
	v_add_f32_e32 v120, 1.0, v120
	v_add_f32_e32 v121, 1.0, v121
	v_rcp_f32_e32 v120, v120
	v_rcp_f32_e32 v121, v121
	v_max_f32_e32 v114, 0x35800000, v114
	v_max_f32_e32 v115, 0x35800000, v115
	v_max_f32_e32 v116, 0x35800000, v116
	v_max_f32_e32 v117, 0x35800000, v117
	v_max_f32_e32 v118, 0x35800000, v118
	v_max_f32_e32 v119, 0x35800000, v119
	v_mul_f32_e32 v108, v108, v114
	v_mul_f32_e32 v109, v109, v115
	v_max_f32_e32 v120, 0x35800000, v120
	v_max_f32_e32 v121, 0x35800000, v121
	v_cvt_pk_bf16_f32 v108, v108, v109
	v_mul_f32_e32 v109, v110, v116
	v_mul_f32_e32 v110, v111, v117
	v_mul_f32_e32 v104, v104, v118
	v_mul_f32_e32 v105, v105, v119
	v_lshlrev_b64 v[112:113], 12, v[170:171]
	v_cvt_pk_bf16_f32 v109, v109, v110
	v_cvt_pk_bf16_f32 v110, v104, v105
	v_mul_f32_e32 v104, v106, v120
	v_mul_f32_e32 v105, v107, v121
	v_cvt_pk_bf16_f32 v111, v104, v105
	v_lshl_add_u64 v[104:105], s[16:17], 0, v[112:113]
	v_lshl_add_u64 v[104:105], v[104:105], 0, v[148:149]
	s_waitcnt vmcnt(6)
	v_lshlrev_b32_e32 v106, 16, v144
	v_and_b32_e32 v107, 0xffff0000, v144
	global_store_dwordx4 v[104:105], v[108:111], off
	v_mul_f32_e32 v106, 0xbfb8aa3b, v106
	v_mul_f32_e32 v107, 0xbfb8aa3b, v107
	v_lshlrev_b32_e32 v108, 16, v145
	v_and_b32_e32 v109, 0xffff0000, v145
	v_lshlrev_b32_e32 v110, 16, v146
	v_and_b32_e32 v111, 0xffff0000, v146
	v_exp_f32_e32 v106, v106
	v_lshlrev_b32_e32 v112, 16, v147
	v_and_b32_e32 v113, 0xffff0000, v147
	v_exp_f32_e32 v107, v107
	v_mul_f32_e32 v108, 0xbfb8aa3b, v108
	v_mul_f32_e32 v109, 0xbfb8aa3b, v109
	v_mul_f32_e32 v110, 0xbfb8aa3b, v110
	v_mul_f32_e32 v111, 0xbfb8aa3b, v111
	v_exp_f32_e32 v108, v108
	v_exp_f32_e32 v109, v109
	v_exp_f32_e32 v110, v110
	v_exp_f32_e32 v111, v111
	v_mul_f32_e32 v112, 0xbfb8aa3b, v112
	v_mul_f32_e32 v113, 0xbfb8aa3b, v113
	v_exp_f32_e32 v112, v112
	v_exp_f32_e32 v113, v113
	v_add_f32_e32 v106, 1.0, v106
	v_add_f32_e32 v107, 1.0, v107
	v_rcp_f32_e32 v106, v106
	v_rcp_f32_e32 v107, v107
	v_add_f32_e32 v108, 1.0, v108
	v_add_f32_e32 v109, 1.0, v109
	v_add_f32_e32 v110, 1.0, v110
	v_add_f32_e32 v111, 1.0, v111
	v_rcp_f32_e32 v108, v108
	v_rcp_f32_e32 v109, v109
	v_rcp_f32_e32 v110, v110
	v_rcp_f32_e32 v111, v111
	v_add_f32_e32 v112, 1.0, v112
	v_add_f32_e32 v113, 1.0, v113
	v_rcp_f32_e32 v112, v112
	v_rcp_f32_e32 v113, v113
	v_max_f32_e32 v106, 0x35800000, v106
	v_max_f32_e32 v107, 0x35800000, v107
	v_max_f32_e32 v108, 0x35800000, v108
	v_max_f32_e32 v109, 0x35800000, v109
	v_max_f32_e32 v110, 0x35800000, v110
	v_max_f32_e32 v111, 0x35800000, v111
	v_mul_f32_e32 v100, v100, v106
	v_mul_f32_e32 v101, v101, v107
	v_max_f32_e32 v112, 0x35800000, v112
	v_max_f32_e32 v113, 0x35800000, v113
	v_cvt_pk_bf16_f32 v100, v100, v101
	v_mul_f32_e32 v101, v102, v108
	v_mul_f32_e32 v102, v103, v109
	v_mul_f32_e32 v96, v96, v110
	v_mul_f32_e32 v97, v97, v111
	v_cvt_pk_bf16_f32 v101, v101, v102
	v_cvt_pk_bf16_f32 v102, v96, v97
	v_mul_f32_e32 v96, v98, v112
	v_mul_f32_e32 v97, v99, v113
	v_cvt_pk_bf16_f32 v103, v96, v97
	s_waitcnt vmcnt(6)
	v_lshlrev_b32_e32 v98, 16, v140
	v_and_b32_e32 v99, 0xffff0000, v140
	global_store_dwordx4 v[104:105], v[100:103], off offset:256
	v_mul_f32_e32 v98, 0xbfb8aa3b, v98
	v_mul_f32_e32 v99, 0xbfb8aa3b, v99
	v_lshlrev_b32_e32 v100, 16, v141
	v_and_b32_e32 v101, 0xffff0000, v141
	v_lshlrev_b32_e32 v102, 16, v142
	v_and_b32_e32 v103, 0xffff0000, v142
	v_exp_f32_e32 v98, v98
	v_lshlrev_b32_e32 v104, 16, v143
	v_and_b32_e32 v105, 0xffff0000, v143
	v_exp_f32_e32 v99, v99
	v_mul_f32_e32 v100, 0xbfb8aa3b, v100
	v_mul_f32_e32 v101, 0xbfb8aa3b, v101
	v_mul_f32_e32 v102, 0xbfb8aa3b, v102
	v_mul_f32_e32 v103, 0xbfb8aa3b, v103
	v_exp_f32_e32 v100, v100
	v_exp_f32_e32 v101, v101
	v_exp_f32_e32 v102, v102
	v_exp_f32_e32 v103, v103
	v_mul_f32_e32 v104, 0xbfb8aa3b, v104
	v_mul_f32_e32 v105, 0xbfb8aa3b, v105
	v_exp_f32_e32 v104, v104
	v_exp_f32_e32 v105, v105
	v_add_f32_e32 v98, 1.0, v98
	v_add_f32_e32 v99, 1.0, v99
	v_rcp_f32_e32 v98, v98
	v_rcp_f32_e32 v99, v99
	v_add_f32_e32 v100, 1.0, v100
	v_add_f32_e32 v101, 1.0, v101
	v_add_f32_e32 v102, 1.0, v102
	v_add_f32_e32 v103, 1.0, v103
	v_rcp_f32_e32 v100, v100
	v_rcp_f32_e32 v101, v101
	v_rcp_f32_e32 v102, v102
	v_rcp_f32_e32 v103, v103
	v_add_f32_e32 v104, 1.0, v104
	v_add_f32_e32 v105, 1.0, v105
	v_rcp_f32_e32 v104, v104
	v_rcp_f32_e32 v105, v105
	v_max_f32_e32 v98, 0x35800000, v98
	v_max_f32_e32 v99, 0x35800000, v99
	v_max_f32_e32 v100, 0x35800000, v100
	v_max_f32_e32 v101, 0x35800000, v101
	v_max_f32_e32 v102, 0x35800000, v102
	v_max_f32_e32 v103, 0x35800000, v103
	v_mul_f32_e32 v92, v92, v98
	v_mul_f32_e32 v93, v93, v99
	v_max_f32_e32 v104, 0x35800000, v104
	v_max_f32_e32 v105, 0x35800000, v105
	v_cvt_pk_bf16_f32 v92, v92, v93
	v_mul_f32_e32 v93, v94, v100
	v_mul_f32_e32 v94, v95, v101
	v_mul_f32_e32 v88, v88, v102
	v_mul_f32_e32 v89, v89, v103
	v_lshlrev_b64 v[96:97], 12, v[168:169]
	v_cvt_pk_bf16_f32 v93, v93, v94
	v_cvt_pk_bf16_f32 v94, v88, v89
	v_mul_f32_e32 v88, v90, v104
	v_mul_f32_e32 v89, v91, v105
	v_cvt_pk_bf16_f32 v95, v88, v89
	v_lshl_add_u64 v[88:89], s[16:17], 0, v[96:97]
	v_lshl_add_u64 v[88:89], v[88:89], 0, v[148:149]
	s_waitcnt vmcnt(6)
	v_lshlrev_b32_e32 v90, 16, v136
	v_and_b32_e32 v91, 0xffff0000, v136
	global_store_dwordx4 v[88:89], v[92:95], off
	v_mul_f32_e32 v90, 0xbfb8aa3b, v90
	v_mul_f32_e32 v91, 0xbfb8aa3b, v91
	v_lshlrev_b32_e32 v92, 16, v137
	v_and_b32_e32 v93, 0xffff0000, v137
	v_lshlrev_b32_e32 v94, 16, v138
	v_and_b32_e32 v95, 0xffff0000, v138
	v_exp_f32_e32 v90, v90
	v_lshlrev_b32_e32 v96, 16, v139
	v_and_b32_e32 v97, 0xffff0000, v139
	v_exp_f32_e32 v91, v91
	v_mul_f32_e32 v92, 0xbfb8aa3b, v92
	v_mul_f32_e32 v93, 0xbfb8aa3b, v93
	v_mul_f32_e32 v94, 0xbfb8aa3b, v94
	v_mul_f32_e32 v95, 0xbfb8aa3b, v95
	v_exp_f32_e32 v92, v92
	v_exp_f32_e32 v93, v93
	v_exp_f32_e32 v94, v94
	v_exp_f32_e32 v95, v95
	v_mul_f32_e32 v96, 0xbfb8aa3b, v96
	v_mul_f32_e32 v97, 0xbfb8aa3b, v97
	v_exp_f32_e32 v96, v96
	v_exp_f32_e32 v97, v97
	v_add_f32_e32 v90, 1.0, v90
	v_add_f32_e32 v91, 1.0, v91
	v_rcp_f32_e32 v90, v90
	v_rcp_f32_e32 v91, v91
	v_add_f32_e32 v92, 1.0, v92
	v_add_f32_e32 v93, 1.0, v93
	v_add_f32_e32 v94, 1.0, v94
	v_add_f32_e32 v95, 1.0, v95
	v_rcp_f32_e32 v92, v92
	v_rcp_f32_e32 v93, v93
	v_rcp_f32_e32 v94, v94
	v_rcp_f32_e32 v95, v95
	v_add_f32_e32 v96, 1.0, v96
	v_add_f32_e32 v97, 1.0, v97
	v_rcp_f32_e32 v96, v96
	v_rcp_f32_e32 v97, v97
	v_max_f32_e32 v90, 0x35800000, v90
	v_max_f32_e32 v91, 0x35800000, v91
	v_max_f32_e32 v92, 0x35800000, v92
	v_max_f32_e32 v93, 0x35800000, v93
	v_max_f32_e32 v94, 0x35800000, v94
	v_max_f32_e32 v95, 0x35800000, v95
	v_mul_f32_e32 v84, v84, v90
	v_mul_f32_e32 v85, v85, v91
	v_max_f32_e32 v96, 0x35800000, v96
	v_max_f32_e32 v97, 0x35800000, v97
	v_cvt_pk_bf16_f32 v84, v84, v85
	v_mul_f32_e32 v85, v86, v92
	v_mul_f32_e32 v86, v87, v93
	v_mul_f32_e32 v80, v80, v94
	v_mul_f32_e32 v81, v81, v95
	v_cvt_pk_bf16_f32 v85, v85, v86
	v_cvt_pk_bf16_f32 v86, v80, v81
	v_mul_f32_e32 v80, v82, v96
	v_mul_f32_e32 v81, v83, v97
	v_cvt_pk_bf16_f32 v87, v80, v81
	s_waitcnt vmcnt(6)
	v_lshlrev_b32_e32 v82, 16, v132
	v_and_b32_e32 v83, 0xffff0000, v132
	global_store_dwordx4 v[88:89], v[84:87], off offset:256
	v_mul_f32_e32 v82, 0xbfb8aa3b, v82
	v_mul_f32_e32 v83, 0xbfb8aa3b, v83
	v_lshlrev_b32_e32 v84, 16, v133
	v_and_b32_e32 v85, 0xffff0000, v133
	v_lshlrev_b32_e32 v86, 16, v134
	v_and_b32_e32 v87, 0xffff0000, v134
	v_exp_f32_e32 v82, v82
	v_lshlrev_b32_e32 v88, 16, v135
	v_and_b32_e32 v89, 0xffff0000, v135
	v_exp_f32_e32 v83, v83
	v_mul_f32_e32 v84, 0xbfb8aa3b, v84
	v_mul_f32_e32 v85, 0xbfb8aa3b, v85
	v_mul_f32_e32 v86, 0xbfb8aa3b, v86
	v_mul_f32_e32 v87, 0xbfb8aa3b, v87
	v_exp_f32_e32 v84, v84
	v_exp_f32_e32 v85, v85
	v_exp_f32_e32 v86, v86
	v_exp_f32_e32 v87, v87
	v_mul_f32_e32 v88, 0xbfb8aa3b, v88
	v_mul_f32_e32 v89, 0xbfb8aa3b, v89
	v_exp_f32_e32 v88, v88
	v_exp_f32_e32 v89, v89
	v_add_f32_e32 v82, 1.0, v82
	v_add_f32_e32 v83, 1.0, v83
	v_rcp_f32_e32 v82, v82
	v_rcp_f32_e32 v83, v83
	v_add_f32_e32 v84, 1.0, v84
	v_add_f32_e32 v85, 1.0, v85
	v_add_f32_e32 v86, 1.0, v86
	v_add_f32_e32 v87, 1.0, v87
	v_rcp_f32_e32 v84, v84
	v_rcp_f32_e32 v85, v85
	v_rcp_f32_e32 v86, v86
	v_rcp_f32_e32 v87, v87
	v_add_f32_e32 v88, 1.0, v88
	v_add_f32_e32 v89, 1.0, v89
	v_rcp_f32_e32 v88, v88
	v_rcp_f32_e32 v89, v89
	v_max_f32_e32 v82, 0x35800000, v82
	v_max_f32_e32 v83, 0x35800000, v83
	v_max_f32_e32 v84, 0x35800000, v84
	v_max_f32_e32 v85, 0x35800000, v85
	v_max_f32_e32 v86, 0x35800000, v86
	v_max_f32_e32 v87, 0x35800000, v87
	v_mul_f32_e32 v76, v76, v82
	v_mul_f32_e32 v77, v77, v83
	v_max_f32_e32 v88, 0x35800000, v88
	v_max_f32_e32 v89, 0x35800000, v89
	v_cvt_pk_bf16_f32 v76, v76, v77
	v_mul_f32_e32 v77, v78, v84
	v_mul_f32_e32 v78, v79, v85
	v_mul_f32_e32 v72, v72, v86
	v_mul_f32_e32 v73, v73, v87
	v_lshlrev_b64 v[80:81], 12, v[166:167]
	v_cvt_pk_bf16_f32 v77, v77, v78
	v_cvt_pk_bf16_f32 v78, v72, v73
	v_mul_f32_e32 v72, v74, v88
	v_mul_f32_e32 v73, v75, v89
	v_cvt_pk_bf16_f32 v79, v72, v73
	v_lshl_add_u64 v[72:73], s[16:17], 0, v[80:81]
	v_lshl_add_u64 v[72:73], v[72:73], 0, v[148:149]
	s_waitcnt vmcnt(6)
	v_lshlrev_b32_e32 v74, 16, v128
	v_and_b32_e32 v75, 0xffff0000, v128
	global_store_dwordx4 v[72:73], v[76:79], off
	v_mul_f32_e32 v74, 0xbfb8aa3b, v74
	v_mul_f32_e32 v75, 0xbfb8aa3b, v75
	v_lshlrev_b32_e32 v76, 16, v129
	v_and_b32_e32 v77, 0xffff0000, v129
	v_lshlrev_b32_e32 v78, 16, v130
	v_and_b32_e32 v79, 0xffff0000, v130
	v_exp_f32_e32 v74, v74
	v_lshlrev_b32_e32 v80, 16, v131
	v_and_b32_e32 v81, 0xffff0000, v131
	v_exp_f32_e32 v75, v75
	v_mul_f32_e32 v76, 0xbfb8aa3b, v76
	v_mul_f32_e32 v77, 0xbfb8aa3b, v77
	v_mul_f32_e32 v78, 0xbfb8aa3b, v78
	v_mul_f32_e32 v79, 0xbfb8aa3b, v79
	v_exp_f32_e32 v76, v76
	v_exp_f32_e32 v77, v77
	v_exp_f32_e32 v78, v78
	v_exp_f32_e32 v79, v79
	v_mul_f32_e32 v80, 0xbfb8aa3b, v80
	v_mul_f32_e32 v81, 0xbfb8aa3b, v81
	v_exp_f32_e32 v80, v80
	v_exp_f32_e32 v81, v81
	v_add_f32_e32 v74, 1.0, v74
	v_add_f32_e32 v75, 1.0, v75
	v_rcp_f32_e32 v74, v74
	v_rcp_f32_e32 v75, v75
	v_add_f32_e32 v76, 1.0, v76
	v_add_f32_e32 v77, 1.0, v77
	v_add_f32_e32 v78, 1.0, v78
	v_add_f32_e32 v79, 1.0, v79
	v_rcp_f32_e32 v76, v76
	v_rcp_f32_e32 v77, v77
	v_rcp_f32_e32 v78, v78
	v_rcp_f32_e32 v79, v79
	v_add_f32_e32 v80, 1.0, v80
	v_add_f32_e32 v81, 1.0, v81
	v_rcp_f32_e32 v80, v80
	v_rcp_f32_e32 v81, v81
	v_max_f32_e32 v74, 0x35800000, v74
	v_max_f32_e32 v75, 0x35800000, v75
	v_max_f32_e32 v76, 0x35800000, v76
	v_max_f32_e32 v77, 0x35800000, v77
	v_max_f32_e32 v78, 0x35800000, v78
	v_max_f32_e32 v79, 0x35800000, v79
	v_mul_f32_e32 v68, v68, v74
	v_mul_f32_e32 v69, v69, v75
	v_max_f32_e32 v80, 0x35800000, v80
	v_max_f32_e32 v81, 0x35800000, v81
	v_cvt_pk_bf16_f32 v68, v68, v69
	v_mul_f32_e32 v69, v70, v76
	v_mul_f32_e32 v70, v71, v77
	v_mul_f32_e32 v64, v64, v78
	v_mul_f32_e32 v65, v65, v79
	v_cvt_pk_bf16_f32 v69, v69, v70
	v_cvt_pk_bf16_f32 v70, v64, v65
	v_mul_f32_e32 v64, v66, v80
	v_mul_f32_e32 v65, v67, v81
	v_cvt_pk_bf16_f32 v71, v64, v65
	global_load_dwordx4 v[84:87], v[158:159], off
	v_lshlrev_b64 v[96:97], 12, v[156:157]
	global_store_dwordx4 v[72:73], v[68:71], off offset:256
	global_load_dwordx4 v[88:91], v[158:159], off offset:256
	global_load_dwordx4 v[92:95], v[160:161], off
	global_load_dwordx4 v[80:83], v[160:161], off offset:256
	global_load_dwordx4 v[76:79], v[162:163], off
	s_nop 0
	global_load_dwordx4 v[72:75], v[162:163], off offset:256
	global_load_dwordx4 v[68:71], v[164:165], off
	global_load_dwordx4 v[64:67], v[164:165], off offset:256
	s_waitcnt vmcnt(8)
	v_lshlrev_b32_e32 v98, 16, v84
	v_and_b32_e32 v84, 0xffff0000, v84
	v_lshlrev_b32_e32 v99, 16, v85
	v_and_b32_e32 v85, 0xffff0000, v85
	v_lshlrev_b32_e32 v100, 16, v86
	v_mul_f32_e32 v98, 0xbfb8aa3b, v98
	v_and_b32_e32 v86, 0xffff0000, v86
	v_mul_f32_e32 v84, 0xbfb8aa3b, v84
	v_exp_f32_e32 v98, v98
	v_lshlrev_b32_e32 v101, 16, v87
	v_and_b32_e32 v87, 0xffff0000, v87
	v_exp_f32_e32 v84, v84
	v_mul_f32_e32 v99, 0xbfb8aa3b, v99
	v_mul_f32_e32 v85, 0xbfb8aa3b, v85
	v_mul_f32_e32 v100, 0xbfb8aa3b, v100
	v_mul_f32_e32 v86, 0xbfb8aa3b, v86
	v_exp_f32_e32 v99, v99
	v_exp_f32_e32 v85, v85
	v_exp_f32_e32 v100, v100
	v_exp_f32_e32 v86, v86
	v_mul_f32_e32 v101, 0xbfb8aa3b, v101
	v_mul_f32_e32 v87, 0xbfb8aa3b, v87
	v_exp_f32_e32 v101, v101
	v_exp_f32_e32 v87, v87
	v_add_f32_e32 v98, 1.0, v98
	v_add_f32_e32 v84, 1.0, v84
	v_rcp_f32_e32 v98, v98
	v_rcp_f32_e32 v84, v84
	v_add_f32_e32 v99, 1.0, v99
	v_add_f32_e32 v85, 1.0, v85
	v_add_f32_e32 v100, 1.0, v100
	v_add_f32_e32 v86, 1.0, v86
	v_rcp_f32_e32 v99, v99
	v_rcp_f32_e32 v85, v85
	v_rcp_f32_e32 v100, v100
	v_rcp_f32_e32 v86, v86
	v_add_f32_e32 v101, 1.0, v101
	v_add_f32_e32 v87, 1.0, v87
	v_rcp_f32_e32 v101, v101
	v_rcp_f32_e32 v87, v87
	v_max_f32_e32 v98, 0x35800000, v98
	v_max_f32_e32 v84, 0x35800000, v84
	v_max_f32_e32 v99, 0x35800000, v99
	v_max_f32_e32 v85, 0x35800000, v85
	v_max_f32_e32 v100, 0x35800000, v100
	v_max_f32_e32 v86, 0x35800000, v86
	v_mul_f32_e32 v60, v60, v98
	v_mul_f32_e32 v61, v61, v84
	v_max_f32_e32 v101, 0x35800000, v101
	v_max_f32_e32 v87, 0x35800000, v87
	v_cvt_pk_bf16_f32 v60, v60, v61
	v_mul_f32_e32 v61, v62, v99
	v_mul_f32_e32 v62, v63, v85
	v_mul_f32_e32 v56, v56, v100
	v_mul_f32_e32 v57, v57, v86
	v_cvt_pk_bf16_f32 v61, v61, v62
	v_cvt_pk_bf16_f32 v62, v56, v57
	v_mul_f32_e32 v56, v58, v101
	v_mul_f32_e32 v57, v59, v87
	v_cvt_pk_bf16_f32 v63, v56, v57
	v_lshl_add_u64 v[56:57], s[16:17], 0, v[96:97]
	v_lshl_add_u64 v[56:57], v[56:57], 0, v[148:149]
	s_waitcnt vmcnt(6)
	v_lshlrev_b32_e32 v58, 16, v88
	v_and_b32_e32 v59, 0xffff0000, v88
	global_store_dwordx4 v[56:57], v[60:63], off
	v_mul_f32_e32 v58, 0xbfb8aa3b, v58
	v_mul_f32_e32 v59, 0xbfb8aa3b, v59
	v_lshlrev_b32_e32 v60, 16, v89
	v_and_b32_e32 v61, 0xffff0000, v89
	v_lshlrev_b32_e32 v62, 16, v90
	v_and_b32_e32 v63, 0xffff0000, v90
	v_exp_f32_e32 v58, v58
	v_lshlrev_b32_e32 v84, 16, v91
	v_and_b32_e32 v85, 0xffff0000, v91
	v_exp_f32_e32 v59, v59
	v_mul_f32_e32 v60, 0xbfb8aa3b, v60
	v_mul_f32_e32 v61, 0xbfb8aa3b, v61
	v_mul_f32_e32 v62, 0xbfb8aa3b, v62
	v_mul_f32_e32 v63, 0xbfb8aa3b, v63
	v_exp_f32_e32 v60, v60
	v_exp_f32_e32 v61, v61
	v_exp_f32_e32 v62, v62
	v_exp_f32_e32 v63, v63
	v_mul_f32_e32 v84, 0xbfb8aa3b, v84
	v_mul_f32_e32 v85, 0xbfb8aa3b, v85
	v_exp_f32_e32 v84, v84
	v_exp_f32_e32 v85, v85
	v_add_f32_e32 v58, 1.0, v58
	v_add_f32_e32 v59, 1.0, v59
	v_rcp_f32_e32 v58, v58
	v_rcp_f32_e32 v59, v59
	v_add_f32_e32 v60, 1.0, v60
	v_add_f32_e32 v61, 1.0, v61
	v_add_f32_e32 v62, 1.0, v62
	v_add_f32_e32 v63, 1.0, v63
	v_rcp_f32_e32 v60, v60
	v_rcp_f32_e32 v61, v61
	v_rcp_f32_e32 v62, v62
	v_rcp_f32_e32 v63, v63
	v_add_f32_e32 v84, 1.0, v84
	v_add_f32_e32 v85, 1.0, v85
	v_rcp_f32_e32 v84, v84
	v_rcp_f32_e32 v85, v85
	v_max_f32_e32 v58, 0x35800000, v58
	v_max_f32_e32 v59, 0x35800000, v59
	v_max_f32_e32 v60, 0x35800000, v60
	v_max_f32_e32 v61, 0x35800000, v61
	v_max_f32_e32 v62, 0x35800000, v62
	v_max_f32_e32 v63, 0x35800000, v63
	v_mul_f32_e32 v52, v52, v58
	v_mul_f32_e32 v53, v53, v59
	v_max_f32_e32 v84, 0x35800000, v84
	v_max_f32_e32 v85, 0x35800000, v85
	v_cvt_pk_bf16_f32 v52, v52, v53
	v_mul_f32_e32 v53, v54, v60
	v_mul_f32_e32 v54, v55, v61
	v_mul_f32_e32 v48, v48, v62
	v_mul_f32_e32 v49, v49, v63
	v_cvt_pk_bf16_f32 v53, v53, v54
	v_cvt_pk_bf16_f32 v54, v48, v49
	v_mul_f32_e32 v48, v50, v84
	v_mul_f32_e32 v49, v51, v85
	v_cvt_pk_bf16_f32 v55, v48, v49
	s_waitcnt vmcnt(6)
	v_lshlrev_b32_e32 v50, 16, v92
	v_and_b32_e32 v51, 0xffff0000, v92
	global_store_dwordx4 v[56:57], v[52:55], off offset:256
	v_mul_f32_e32 v50, 0xbfb8aa3b, v50
	v_mul_f32_e32 v51, 0xbfb8aa3b, v51
	v_lshlrev_b32_e32 v52, 16, v93
	v_and_b32_e32 v53, 0xffff0000, v93
	v_lshlrev_b32_e32 v54, 16, v94
	v_and_b32_e32 v55, 0xffff0000, v94
	v_exp_f32_e32 v50, v50
	v_lshlrev_b32_e32 v56, 16, v95
	v_and_b32_e32 v57, 0xffff0000, v95
	v_exp_f32_e32 v51, v51
	v_mul_f32_e32 v52, 0xbfb8aa3b, v52
	v_mul_f32_e32 v53, 0xbfb8aa3b, v53
	v_mul_f32_e32 v54, 0xbfb8aa3b, v54
	v_mul_f32_e32 v55, 0xbfb8aa3b, v55
	v_exp_f32_e32 v52, v52
	v_exp_f32_e32 v53, v53
	v_exp_f32_e32 v54, v54
	v_exp_f32_e32 v55, v55
	v_mul_f32_e32 v56, 0xbfb8aa3b, v56
	v_mul_f32_e32 v57, 0xbfb8aa3b, v57
	v_exp_f32_e32 v56, v56
	v_exp_f32_e32 v57, v57
	v_add_f32_e32 v50, 1.0, v50
	v_add_f32_e32 v51, 1.0, v51
	v_rcp_f32_e32 v50, v50
	v_rcp_f32_e32 v51, v51
	v_add_f32_e32 v52, 1.0, v52
	v_add_f32_e32 v53, 1.0, v53
	v_add_f32_e32 v54, 1.0, v54
	v_add_f32_e32 v55, 1.0, v55
	v_rcp_f32_e32 v52, v52
	v_rcp_f32_e32 v53, v53
	v_rcp_f32_e32 v54, v54
	v_rcp_f32_e32 v55, v55
	v_add_f32_e32 v56, 1.0, v56
	v_add_f32_e32 v57, 1.0, v57
	v_rcp_f32_e32 v56, v56
	v_rcp_f32_e32 v57, v57
	v_max_f32_e32 v50, 0x35800000, v50
	v_max_f32_e32 v51, 0x35800000, v51
	v_max_f32_e32 v52, 0x35800000, v52
	v_max_f32_e32 v53, 0x35800000, v53
	v_max_f32_e32 v54, 0x35800000, v54
	v_max_f32_e32 v55, 0x35800000, v55
	v_mul_f32_e32 v44, v44, v50
	v_mul_f32_e32 v45, v45, v51
	v_max_f32_e32 v56, 0x35800000, v56
	v_max_f32_e32 v57, 0x35800000, v57
	v_cvt_pk_bf16_f32 v44, v44, v45
	v_mul_f32_e32 v45, v46, v52
	v_mul_f32_e32 v46, v47, v53
	v_mul_f32_e32 v40, v40, v54
	v_mul_f32_e32 v41, v41, v55
	v_lshlrev_b64 v[48:49], 12, v[154:155]
	v_cvt_pk_bf16_f32 v45, v45, v46
	v_cvt_pk_bf16_f32 v46, v40, v41
	v_mul_f32_e32 v40, v42, v56
	v_mul_f32_e32 v41, v43, v57
	v_cvt_pk_bf16_f32 v47, v40, v41
	v_lshl_add_u64 v[40:41], s[16:17], 0, v[48:49]
	v_lshl_add_u64 v[40:41], v[40:41], 0, v[148:149]
	s_waitcnt vmcnt(6)
	v_lshlrev_b32_e32 v42, 16, v80
	v_and_b32_e32 v43, 0xffff0000, v80
	global_store_dwordx4 v[40:41], v[44:47], off
	v_mul_f32_e32 v42, 0xbfb8aa3b, v42
	v_mul_f32_e32 v43, 0xbfb8aa3b, v43
	v_lshlrev_b32_e32 v44, 16, v81
	v_and_b32_e32 v45, 0xffff0000, v81
	v_lshlrev_b32_e32 v46, 16, v82
	v_and_b32_e32 v47, 0xffff0000, v82
	v_exp_f32_e32 v42, v42
	v_lshlrev_b32_e32 v48, 16, v83
	v_and_b32_e32 v49, 0xffff0000, v83
	v_exp_f32_e32 v43, v43
	v_mul_f32_e32 v44, 0xbfb8aa3b, v44
	v_mul_f32_e32 v45, 0xbfb8aa3b, v45
	v_mul_f32_e32 v46, 0xbfb8aa3b, v46
	v_mul_f32_e32 v47, 0xbfb8aa3b, v47
	v_exp_f32_e32 v44, v44
	v_exp_f32_e32 v45, v45
	v_exp_f32_e32 v46, v46
	v_exp_f32_e32 v47, v47
	v_mul_f32_e32 v48, 0xbfb8aa3b, v48
	v_mul_f32_e32 v49, 0xbfb8aa3b, v49
	v_exp_f32_e32 v48, v48
	v_exp_f32_e32 v49, v49
	v_add_f32_e32 v42, 1.0, v42
	v_add_f32_e32 v43, 1.0, v43
	v_rcp_f32_e32 v42, v42
	v_rcp_f32_e32 v43, v43
	v_add_f32_e32 v44, 1.0, v44
	v_add_f32_e32 v45, 1.0, v45
	v_add_f32_e32 v46, 1.0, v46
	v_add_f32_e32 v47, 1.0, v47
	v_rcp_f32_e32 v44, v44
	v_rcp_f32_e32 v45, v45
	v_rcp_f32_e32 v46, v46
	v_rcp_f32_e32 v47, v47
	v_add_f32_e32 v48, 1.0, v48
	v_add_f32_e32 v49, 1.0, v49
	v_rcp_f32_e32 v48, v48
	v_rcp_f32_e32 v49, v49
	v_max_f32_e32 v42, 0x35800000, v42
	v_max_f32_e32 v43, 0x35800000, v43
	v_max_f32_e32 v44, 0x35800000, v44
	v_max_f32_e32 v45, 0x35800000, v45
	v_max_f32_e32 v46, 0x35800000, v46
	v_max_f32_e32 v47, 0x35800000, v47
	v_mul_f32_e32 v36, v36, v42
	v_mul_f32_e32 v37, v37, v43
	v_max_f32_e32 v48, 0x35800000, v48
	v_max_f32_e32 v49, 0x35800000, v49
	v_cvt_pk_bf16_f32 v36, v36, v37
	v_mul_f32_e32 v37, v38, v44
	v_mul_f32_e32 v38, v39, v45
	v_mul_f32_e32 v32, v32, v46
	v_mul_f32_e32 v33, v33, v47
	v_cvt_pk_bf16_f32 v37, v37, v38
	v_cvt_pk_bf16_f32 v38, v32, v33
	v_mul_f32_e32 v32, v34, v48
	v_mul_f32_e32 v33, v35, v49
	v_cvt_pk_bf16_f32 v39, v32, v33
	s_waitcnt vmcnt(6)
	v_lshlrev_b32_e32 v34, 16, v76
	v_and_b32_e32 v35, 0xffff0000, v76
	global_store_dwordx4 v[40:41], v[36:39], off offset:256
	v_mul_f32_e32 v34, 0xbfb8aa3b, v34
	v_mul_f32_e32 v35, 0xbfb8aa3b, v35
	v_lshlrev_b32_e32 v36, 16, v77
	v_and_b32_e32 v37, 0xffff0000, v77
	v_lshlrev_b32_e32 v38, 16, v78
	v_and_b32_e32 v39, 0xffff0000, v78
	v_exp_f32_e32 v34, v34
	v_lshlrev_b32_e32 v40, 16, v79
	v_and_b32_e32 v41, 0xffff0000, v79
	v_exp_f32_e32 v35, v35
	v_mul_f32_e32 v36, 0xbfb8aa3b, v36
	v_mul_f32_e32 v37, 0xbfb8aa3b, v37
	v_mul_f32_e32 v38, 0xbfb8aa3b, v38
	v_mul_f32_e32 v39, 0xbfb8aa3b, v39
	v_exp_f32_e32 v36, v36
	v_exp_f32_e32 v37, v37
	v_exp_f32_e32 v38, v38
	v_exp_f32_e32 v39, v39
	v_mul_f32_e32 v40, 0xbfb8aa3b, v40
	v_mul_f32_e32 v41, 0xbfb8aa3b, v41
	v_exp_f32_e32 v40, v40
	v_exp_f32_e32 v41, v41
	v_add_f32_e32 v34, 1.0, v34
	v_add_f32_e32 v35, 1.0, v35
	v_rcp_f32_e32 v34, v34
	v_rcp_f32_e32 v35, v35
	v_add_f32_e32 v36, 1.0, v36
	v_add_f32_e32 v37, 1.0, v37
	v_add_f32_e32 v38, 1.0, v38
	v_add_f32_e32 v39, 1.0, v39
	v_rcp_f32_e32 v36, v36
	v_rcp_f32_e32 v37, v37
	v_rcp_f32_e32 v38, v38
	v_rcp_f32_e32 v39, v39
	v_add_f32_e32 v40, 1.0, v40
	v_add_f32_e32 v41, 1.0, v41
	v_rcp_f32_e32 v40, v40
	v_rcp_f32_e32 v41, v41
	v_max_f32_e32 v34, 0x35800000, v34
	v_max_f32_e32 v35, 0x35800000, v35
	v_max_f32_e32 v36, 0x35800000, v36
	v_max_f32_e32 v37, 0x35800000, v37
	v_max_f32_e32 v38, 0x35800000, v38
	v_max_f32_e32 v39, 0x35800000, v39
	v_mul_f32_e32 v28, v28, v34
	v_mul_f32_e32 v29, v29, v35
	v_max_f32_e32 v40, 0x35800000, v40
	v_max_f32_e32 v41, 0x35800000, v41
	v_cvt_pk_bf16_f32 v28, v28, v29
	v_mul_f32_e32 v29, v30, v36
	v_mul_f32_e32 v30, v31, v37
	v_mul_f32_e32 v24, v24, v38
	v_mul_f32_e32 v25, v25, v39
	v_lshlrev_b64 v[32:33], 12, v[152:153]
	v_cvt_pk_bf16_f32 v29, v29, v30
	v_cvt_pk_bf16_f32 v30, v24, v25
	v_mul_f32_e32 v24, v26, v40
	v_mul_f32_e32 v25, v27, v41
	v_cvt_pk_bf16_f32 v31, v24, v25
	v_lshl_add_u64 v[24:25], s[16:17], 0, v[32:33]
	v_lshl_add_u64 v[24:25], v[24:25], 0, v[148:149]
	s_waitcnt vmcnt(6)
	v_lshlrev_b32_e32 v26, 16, v72
	v_and_b32_e32 v27, 0xffff0000, v72
	global_store_dwordx4 v[24:25], v[28:31], off
	v_mul_f32_e32 v26, 0xbfb8aa3b, v26
	v_mul_f32_e32 v27, 0xbfb8aa3b, v27
	v_lshlrev_b32_e32 v28, 16, v73
	v_and_b32_e32 v29, 0xffff0000, v73
	v_lshlrev_b32_e32 v30, 16, v74
	v_and_b32_e32 v31, 0xffff0000, v74
	v_exp_f32_e32 v26, v26
	v_lshlrev_b32_e32 v32, 16, v75
	v_and_b32_e32 v33, 0xffff0000, v75
	v_exp_f32_e32 v27, v27
	v_mul_f32_e32 v28, 0xbfb8aa3b, v28
	v_mul_f32_e32 v29, 0xbfb8aa3b, v29
	v_mul_f32_e32 v30, 0xbfb8aa3b, v30
	v_mul_f32_e32 v31, 0xbfb8aa3b, v31
	v_exp_f32_e32 v28, v28
	v_exp_f32_e32 v29, v29
	v_exp_f32_e32 v30, v30
	v_exp_f32_e32 v31, v31
	v_mul_f32_e32 v32, 0xbfb8aa3b, v32
	v_mul_f32_e32 v33, 0xbfb8aa3b, v33
	v_exp_f32_e32 v32, v32
	v_exp_f32_e32 v33, v33
	v_add_f32_e32 v26, 1.0, v26
	v_add_f32_e32 v27, 1.0, v27
	v_rcp_f32_e32 v26, v26
	v_rcp_f32_e32 v27, v27
	v_add_f32_e32 v28, 1.0, v28
	v_add_f32_e32 v29, 1.0, v29
	v_add_f32_e32 v30, 1.0, v30
	v_add_f32_e32 v31, 1.0, v31
	v_rcp_f32_e32 v28, v28
	v_rcp_f32_e32 v29, v29
	v_rcp_f32_e32 v30, v30
	v_rcp_f32_e32 v31, v31
	v_add_f32_e32 v32, 1.0, v32
	v_add_f32_e32 v33, 1.0, v33
	v_rcp_f32_e32 v32, v32
	v_rcp_f32_e32 v33, v33
	v_max_f32_e32 v26, 0x35800000, v26
	v_max_f32_e32 v27, 0x35800000, v27
	v_max_f32_e32 v28, 0x35800000, v28
	v_max_f32_e32 v29, 0x35800000, v29
	v_max_f32_e32 v30, 0x35800000, v30
	v_max_f32_e32 v31, 0x35800000, v31
	v_mul_f32_e32 v20, v20, v26
	v_mul_f32_e32 v21, v21, v27
	v_max_f32_e32 v32, 0x35800000, v32
	v_max_f32_e32 v33, 0x35800000, v33
	v_cvt_pk_bf16_f32 v20, v20, v21
	v_mul_f32_e32 v21, v22, v28
	v_mul_f32_e32 v22, v23, v29
	v_mul_f32_e32 v16, v16, v30
	v_mul_f32_e32 v17, v17, v31
	v_cvt_pk_bf16_f32 v21, v21, v22
	v_cvt_pk_bf16_f32 v22, v16, v17
	v_mul_f32_e32 v16, v18, v32
	v_mul_f32_e32 v17, v19, v33
	v_cvt_pk_bf16_f32 v23, v16, v17
	s_waitcnt vmcnt(6)
	v_lshlrev_b32_e32 v18, 16, v68
	v_and_b32_e32 v19, 0xffff0000, v68
	global_store_dwordx4 v[24:25], v[20:23], off offset:256
	v_mul_f32_e32 v18, 0xbfb8aa3b, v18
	v_mul_f32_e32 v19, 0xbfb8aa3b, v19
	v_lshlrev_b32_e32 v20, 16, v69
	v_and_b32_e32 v21, 0xffff0000, v69
	v_lshlrev_b32_e32 v22, 16, v70
	v_and_b32_e32 v23, 0xffff0000, v70
	v_exp_f32_e32 v18, v18
	v_lshlrev_b32_e32 v24, 16, v71
	v_and_b32_e32 v25, 0xffff0000, v71
	v_exp_f32_e32 v19, v19
	v_mul_f32_e32 v20, 0xbfb8aa3b, v20
	v_mul_f32_e32 v21, 0xbfb8aa3b, v21
	v_mul_f32_e32 v22, 0xbfb8aa3b, v22
	v_mul_f32_e32 v23, 0xbfb8aa3b, v23
	v_exp_f32_e32 v20, v20
	v_exp_f32_e32 v21, v21
	v_exp_f32_e32 v22, v22
	v_exp_f32_e32 v23, v23
	v_mul_f32_e32 v24, 0xbfb8aa3b, v24
	v_mul_f32_e32 v25, 0xbfb8aa3b, v25
	v_exp_f32_e32 v24, v24
	v_exp_f32_e32 v25, v25
	v_add_f32_e32 v18, 1.0, v18
	v_add_f32_e32 v19, 1.0, v19
	v_rcp_f32_e32 v18, v18
	v_rcp_f32_e32 v19, v19
	v_add_f32_e32 v20, 1.0, v20
	v_add_f32_e32 v21, 1.0, v21
	v_add_f32_e32 v22, 1.0, v22
	v_add_f32_e32 v23, 1.0, v23
	v_rcp_f32_e32 v20, v20
	v_rcp_f32_e32 v21, v21
	v_rcp_f32_e32 v22, v22
	v_rcp_f32_e32 v23, v23
	v_add_f32_e32 v24, 1.0, v24
	v_add_f32_e32 v25, 1.0, v25
	v_rcp_f32_e32 v24, v24
	v_rcp_f32_e32 v25, v25
	v_max_f32_e32 v18, 0x35800000, v18
	v_max_f32_e32 v19, 0x35800000, v19
	v_max_f32_e32 v20, 0x35800000, v20
	v_max_f32_e32 v21, 0x35800000, v21
	v_max_f32_e32 v22, 0x35800000, v22
	v_max_f32_e32 v23, 0x35800000, v23
	v_mul_f32_e32 v12, v12, v18
	v_mul_f32_e32 v13, v13, v19
	v_max_f32_e32 v24, 0x35800000, v24
	v_max_f32_e32 v25, 0x35800000, v25
	v_cvt_pk_bf16_f32 v12, v12, v13
	v_mul_f32_e32 v13, v14, v20
	v_mul_f32_e32 v14, v15, v21
	v_mul_f32_e32 v8, v8, v22
	v_mul_f32_e32 v9, v9, v23
	v_lshlrev_b64 v[16:17], 12, v[150:151]
	v_cvt_pk_bf16_f32 v13, v13, v14
	v_cvt_pk_bf16_f32 v14, v8, v9
	v_mul_f32_e32 v8, v10, v24
	v_mul_f32_e32 v9, v11, v25
	v_cvt_pk_bf16_f32 v15, v8, v9
	v_lshl_add_u64 v[8:9], s[16:17], 0, v[16:17]
	v_lshl_add_u64 v[8:9], v[8:9], 0, v[148:149]
	s_waitcnt vmcnt(6)
	v_lshlrev_b32_e32 v10, 16, v64
	v_and_b32_e32 v11, 0xffff0000, v64
	global_store_dwordx4 v[8:9], v[12:15], off
	v_mul_f32_e32 v10, 0xbfb8aa3b, v10
	v_mul_f32_e32 v11, 0xbfb8aa3b, v11
	v_lshlrev_b32_e32 v12, 16, v65
	v_and_b32_e32 v13, 0xffff0000, v65
	v_lshlrev_b32_e32 v14, 16, v66
	v_exp_f32_e32 v10, v10
	v_and_b32_e32 v15, 0xffff0000, v66
	v_exp_f32_e32 v11, v11
	v_mul_f32_e32 v12, 0xbfb8aa3b, v12
	v_mul_f32_e32 v13, 0xbfb8aa3b, v13
	v_lshlrev_b32_e32 v16, 16, v67
	v_exp_f32_e32 v12, v12
	v_exp_f32_e32 v13, v13
	v_mul_f32_e32 v14, 0xbfb8aa3b, v14
	v_mul_f32_e32 v15, 0xbfb8aa3b, v15
	v_and_b32_e32 v17, 0xffff0000, v67
	v_exp_f32_e32 v14, v14
	v_exp_f32_e32 v15, v15
	v_mul_f32_e32 v16, 0xbfb8aa3b, v16
	v_exp_f32_e32 v16, v16
	v_mul_f32_e32 v17, 0xbfb8aa3b, v17
	v_add_f32_e32 v10, 1.0, v10
	v_add_f32_e32 v11, 1.0, v11
	v_exp_f32_e32 v17, v17
	v_rcp_f32_e32 v10, v10
	v_rcp_f32_e32 v11, v11
	v_add_f32_e32 v12, 1.0, v12
	v_add_f32_e32 v13, 1.0, v13
	v_rcp_f32_e32 v12, v12
	v_rcp_f32_e32 v13, v13
	v_add_f32_e32 v14, 1.0, v14
	v_add_f32_e32 v15, 1.0, v15
	v_rcp_f32_e32 v14, v14
	v_rcp_f32_e32 v15, v15
	v_add_f32_e32 v16, 1.0, v16
	v_rcp_f32_e32 v16, v16
	v_add_f32_e32 v17, 1.0, v17
	v_max_f32_e32 v10, 0x35800000, v10
	v_max_f32_e32 v11, 0x35800000, v11
	v_rcp_f32_e32 v17, v17
	v_max_f32_e32 v12, 0x35800000, v12
	v_max_f32_e32 v13, 0x35800000, v13
	v_mul_f32_e32 v0, v0, v10
	v_mul_f32_e32 v1, v1, v11
	v_max_f32_e32 v14, 0x35800000, v14
	v_max_f32_e32 v15, 0x35800000, v15
	v_cvt_pk_bf16_f32 v0, v0, v1
	v_mul_f32_e32 v1, v2, v12
	v_mul_f32_e32 v2, v3, v13
	v_max_f32_e32 v16, 0x35800000, v16
	v_cvt_pk_bf16_f32 v1, v1, v2
	v_mul_f32_e32 v2, v4, v14
	v_mul_f32_e32 v3, v5, v15
	v_max_f32_e32 v17, 0x35800000, v17
	v_cvt_pk_bf16_f32 v2, v2, v3
	v_mul_f32_e32 v3, v6, v16
	v_mul_f32_e32 v4, v7, v17
	v_cvt_pk_bf16_f32 v3, v3, v4
	global_store_dwordx4 v[8:9], v[0:3], off offset:256
	s_cbranch_vccnz .LBB0_860
	s_andn2_b64 vcc, exec, s[6:7]
	v_mov_b64 v[124:125], 0
	v_mov_b64 v[126:127], 0
	v_mov_b64 v[120:121], 0
	v_mov_b64 v[122:123], 0
	v_mov_b64 v[108:109], 0
	v_mov_b64 v[110:111], 0
	v_mov_b64 v[104:105], 0
	v_mov_b64 v[106:107], 0
	v_mov_b64 v[92:93], 0
	v_mov_b64 v[94:95], 0
	v_mov_b64 v[88:89], 0
	v_mov_b64 v[90:91], 0
	v_mov_b64 v[76:77], 0
	v_mov_b64 v[78:79], 0
	v_mov_b64 v[72:73], 0
	v_mov_b64 v[74:75], 0
	v_mov_b64 v[116:117], 0
	v_mov_b64 v[118:119], 0
	v_mov_b64 v[112:113], 0
	v_mov_b64 v[114:115], 0
	v_mov_b64 v[100:101], 0
	v_mov_b64 v[102:103], 0
	v_mov_b64 v[96:97], 0
	v_mov_b64 v[98:99], 0
	v_mov_b64 v[84:85], 0
	v_mov_b64 v[86:87], 0
	v_mov_b64 v[80:81], 0
	v_mov_b64 v[82:83], 0
	v_mov_b64 v[68:69], 0
	v_mov_b64 v[70:71], 0
	v_mov_b64 v[64:65], 0
	v_mov_b64 v[66:67], 0
	v_mov_b64 v[60:61], 0
	v_mov_b64 v[62:63], 0
	v_mov_b64 v[56:57], 0
	v_mov_b64 v[58:59], 0
	v_mov_b64 v[44:45], 0
	v_mov_b64 v[46:47], 0
	v_mov_b64 v[40:41], 0
	v_mov_b64 v[42:43], 0
	v_mov_b64 v[28:29], 0
	v_mov_b64 v[30:31], 0
	v_mov_b64 v[24:25], 0
	v_mov_b64 v[26:27], 0
	v_mov_b64 v[12:13], 0
	v_mov_b64 v[14:15], 0
	v_mov_b64 v[8:9], 0
	v_mov_b64 v[10:11], 0
	v_mov_b64 v[52:53], 0
	v_mov_b64 v[54:55], 0
	v_mov_b64 v[48:49], 0
	v_mov_b64 v[50:51], 0
	v_mov_b64 v[36:37], 0
	v_mov_b64 v[38:39], 0
	v_mov_b64 v[32:33], 0
	v_mov_b64 v[34:35], 0
	v_mov_b64 v[20:21], 0
	v_mov_b64 v[22:23], 0
	v_mov_b64 v[16:17], 0
	v_mov_b64 v[18:19], 0
	v_mov_b64 v[0:1], 0
	v_mov_b64 v[2:3], 0
	v_mov_b64 v[4:5], 0
	v_mov_b64 v[6:7], 0
	s_cbranch_vccnz .LBB0_859
	s_barrier
	s_branch .LBB0_859

.LBB0_941:
	s_ashr_i32 s2, s4, 3
	s_add_u32 s4, s92, 0x2cee1c00
	s_addc_u32 s3, s93, 0
	v_mbcnt_lo_u32_b32 v0, -1, 0
	s_add_u32 s8, s92, 0x2ce0400
	v_mbcnt_hi_u32_b32 v135, -1, v0
	s_addc_u32 s9, s93, 0
	s_lshl_b32 s13, s86, 10
	v_lshl_or_b32 v0, v135, 4, s13
	v_ashrrev_i32_e32 v1, 31, v0
	v_lshrrev_b32_e32 v1, 22, v1
	v_add_u32_e32 v1, v0, v1
	v_ashrrev_i32_e32 v1, 10, v1
	v_mul_i32_i24_e32 v2, 0x400, v1
	v_sub_u32_e32 v2, v0, v2
	v_lshrrev_b32_e32 v3, 4, v2
	v_bitop3_b32 v2, v3, v2, 32 bitop3:0x6c
	s_waitcnt vmcnt(8)
	v_ashrrev_i32_e32 v4, 31, v2
	v_lshrrev_b32_e32 v4, 26, v4
	v_lshlrev_b32_e32 v3, 3, v1
	v_add_u32_e32 v4, v2, v4
	v_and_b32_e32 v3, -16, v3
	v_ashrrev_i32_e32 v5, 6, v4
	v_add_u32_e32 v132, v5, v3
	v_and_b32_e32 v3, 0xc0, v4
	v_lshlrev_b32_e32 v1, 5, v1
	v_sub_u32_e32 v2, v2, v3
	v_mov_b32_e32 v3, 1
	v_and_b32_e32 v1, 32, v1
	v_ashrrev_i16_sdwa v2, v3, sext(v2) dst_sel:DWORD dst_unused:UNUSED_PAD src0_sel:DWORD src1_sel:BYTE_0
	v_add_u32_sdwa v133, v1, sext(v2) dst_sel:DWORD dst_unused:UNUSED_PAD src0_sel:DWORD src1_sel:WORD_0
	v_lshlrev_b32_e32 v1, 1, v132
	v_lshrrev_b32_e32 v2, 2, v132
	v_and_b32_e32 v4, 3, v5
	s_mov_b32 s5, 0xfffe0
	v_and_b32_e32 v1, 24, v1
	v_and_b32_e32 v2, 4, v2
	v_and_or_b32 v4, v132, s5, v4
	v_or3_b32 v1, v4, v2, v1
	v_lshlrev_b32_e32 v130, 1, v133
	v_add_u32_e32 v0, 0x2000, v0
	v_lshl_add_u32 v128, v1, 12, v130
	v_ashrrev_i32_e32 v1, 31, v0
	v_lshrrev_b32_e32 v1, 22, v1
	v_add_u32_e32 v1, v0, v1
	v_ashrrev_i32_e32 v1, 10, v1
	v_mul_i32_i24_e32 v2, 0x400, v1
	v_sub_u32_e32 v0, v0, v2
	v_lshrrev_b32_e32 v2, 4, v0
	v_bitop3_b32 v0, v2, v0, 32 bitop3:0x6c
	v_ashrrev_i32_e32 v4, 31, v0
	v_lshrrev_b32_e32 v4, 26, v4
	v_lshlrev_b32_e32 v2, 3, v1
	v_add_u32_e32 v4, v0, v4
	v_and_b32_e32 v2, -16, v2
	v_ashrrev_i32_e32 v5, 6, v4
	v_add_u32_e32 v134, v5, v2
	v_and_b32_e32 v2, 0xffc0, v4
	v_sub_u32_e32 v0, v0, v2
	v_lshrrev_b16_e32 v2, 7, v0
	v_and_b32_e32 v2, 1, v2
	v_add_u16_e32 v0, v0, v2
	v_and_b32_e32 v2, 3, v5
	s_add_i32 s2, s12, s2
	v_and_or_b32 v2, v134, s5, v2
	s_and_b32 s5, s3, 0xffff
	s_ashr_i32 s3, s2, 31
	s_lshr_b32 s3, s3, 27
	s_add_i32 s3, s2, s3
	s_ashr_i32 s12, s3, 5
	s_andn2_b32 s3, s3, 31
	s_sub_i32 s2, s2, s3
	s_bfe_i32 s3, s2, 0x80000
	s_bfe_u32 s3, s3, 0x2000d
	v_lshlrev_b32_e32 v1, 5, v1
	s_add_i32 s3, s2, s3
	v_and_b32_e32 v1, 32, v1
	v_ashrrev_i16_sdwa v0, v3, sext(v0) dst_sel:DWORD dst_unused:UNUSED_PAD src0_sel:DWORD src1_sel:BYTE_0
	s_bfe_i32 s14, s3, 0x80000
	v_add_u32_sdwa v136, v1, sext(v0) dst_sel:DWORD dst_unused:UNUSED_PAD src0_sel:DWORD src1_sel:WORD_0
	v_lshlrev_b32_e32 v0, 1, v134
	v_lshrrev_b32_e32 v1, 2, v134
	s_sext_i32_i16 s14, s14
	s_add_i32 s26, s13, 0
	s_mov_b32 s6, -1
	v_and_b32_e32 v0, 24, v0
	v_and_b32_e32 v1, 4, v1
	s_mov_b32 s7, 0x20000
	s_and_b32 s3, s3, 0xfc
	s_ashr_i32 s52, s14, 2
	s_add_i32 s27, s26, 0x10000
	v_or3_b32 v0, v2, v1, v0
	v_lshlrev_b32_e32 v131, 1, v136
	s_and_b32 s9, s9, 0xffff
	s_mov_b32 s10, s6
	s_mov_b32 s11, s7
	s_sub_i32 s2, s2, s3
	s_lshl_b32 s55, s52, 20
	s_mov_b32 m0, s27
	s_add_i32 s28, s26, 0x12000
	v_lshl_add_u32 v129, v0, 12, v131
	s_lshl_b32 s12, s12, 2
	s_sext_i32_i8 s2, s2
	v_mov_b64 v[120:121], 0
	v_mov_b64 v[122:123], 0
	v_mov_b64 v[112:113], 0
	v_mov_b64 v[114:115], 0
	v_mov_b64 v[100:101], 0
	v_mov_b64 v[102:103], 0
	v_mov_b64 v[96:97], 0
	v_mov_b64 v[98:99], 0
	v_mov_b64 v[84:85], 0
	v_mov_b64 v[86:87], 0
	v_mov_b64 v[80:81], 0
	v_mov_b64 v[82:83], 0
	v_mov_b64 v[68:69], 0
	v_mov_b64 v[70:71], 0
	v_mov_b64 v[64:65], 0
	v_mov_b64 v[66:67], 0
	v_mov_b64 v[124:125], 0
	v_mov_b64 v[126:127], 0
	v_mov_b64 v[116:117], 0
	v_mov_b64 v[118:119], 0
	v_mov_b64 v[108:109], 0
	v_mov_b64 v[110:111], 0
	v_mov_b64 v[104:105], 0
	v_mov_b64 v[106:107], 0
	v_mov_b64 v[92:93], 0
	v_mov_b64 v[94:95], 0
	v_mov_b64 v[88:89], 0
	v_mov_b64 v[90:91], 0
	v_mov_b64 v[76:77], 0
	v_mov_b64 v[78:79], 0
	v_mov_b64 v[72:73], 0
	v_mov_b64 v[74:75], 0
	s_waitcnt vmcnt(4)
	v_mov_b64 v[56:57], 0
	v_mov_b64 v[58:59], 0
	v_mov_b64 v[48:49], 0
	v_mov_b64 v[50:51], 0
	v_mov_b64 v[40:41], 0
	v_mov_b64 v[42:43], 0
	v_mov_b64 v[32:33], 0
	v_mov_b64 v[34:35], 0
	v_mov_b64 v[24:25], 0
	v_mov_b64 v[26:27], 0
	v_mov_b64 v[16:17], 0
	v_mov_b64 v[18:19], 0
	v_mov_b64 v[4:5], 0
	v_mov_b64 v[6:7], 0
	v_mov_b64 v[0:1], 0
	v_mov_b64 v[2:3], 0
	v_mov_b64 v[60:61], 0
	v_mov_b64 v[62:63], 0
	v_mov_b64 v[52:53], 0
	v_mov_b64 v[54:55], 0
	v_mov_b64 v[44:45], 0
	v_mov_b64 v[46:47], 0
	v_mov_b64 v[36:37], 0
	v_mov_b64 v[38:39], 0
	v_mov_b64 v[28:29], 0
	v_mov_b64 v[30:31], 0
	v_mov_b64 v[20:21], 0
	v_mov_b64 v[22:23], 0
	v_mov_b64 v[8:9], 0
	v_mov_b64 v[10:11], 0
	v_mov_b64 v[12:13], 0
	v_mov_b64 v[14:15], 0
	buffer_load_dwordx4 v128, s[8:11], s55 offen lds
	s_mov_b32 m0, s28
	s_add_i32 s29, s26, 0x14000
	s_add_i32 s53, s12, s2
	buffer_load_dwordx4 v129, s[8:11], s55 offen lds
	s_or_b32 s2, s55, 0x80000
	s_mov_b32 m0, s29
	s_add_i32 s30, s26, 0x16000
	buffer_load_dwordx4 v128, s[8:11], s2 offen lds
	s_mov_b32 m0, s30
	v_lshl_add_u32 v130, v132, 12, v130
	s_lshl_b32 s54, s53, 20
	buffer_load_dwordx4 v129, s[8:11], s2 offen lds
	s_mov_b32 m0, s26
	s_add_i32 s31, s26, 0x2000
	v_lshl_add_u32 v131, v134, 12, v131
	v_lshl_add_u32 v132, v132, 11, v133
	v_mov_b32_e32 v133, 0x80000
	buffer_load_dwordx4 v130, s[4:7], s54 offen lds
	s_mov_b32 m0, s31
	s_add_i32 s33, s26, 0x4000
	v_lshl_add_u32 v132, v132, 1, v133
	v_lshl_add_u32 v134, v134, 11, v136
	buffer_load_dwordx4 v131, s[4:7], s54 offen lds
	s_mov_b32 m0, s33
	s_add_i32 s34, s26, 0x6000
	v_lshl_add_u32 v133, v134, 1, v133
	buffer_load_dwordx4 v132, s[4:7], s54 offen lds
	s_mov_b32 m0, s34
	s_lshr_b32 s2, s90, 8
	buffer_load_dwordx4 v133, s[4:7], s54 offen lds
	s_cmp_eq_u32 s2, 1
	s_mov_b32 s35, 0
	s_cselect_b64 s[12:13], -1, 0
	s_cmp_lg_u32 s2, 1
	s_mov_b32 s36, 0x80000
	s_cbranch_scc1 .LBB0_943
	s_barrier

.LBB0_958:
	v_lshl_add_u32 v138, s53, 8, v134
	v_lshl_or_b32 v140, s52, 8, v135
	v_ashrrev_i32_e32 v139, 31, v138
	v_ashrrev_i32_e32 v141, 31, v140
	v_cvt_pk_bf16_f32 v120, v120, v121
	v_cvt_pk_bf16_f32 v121, v122, v123
	v_cvt_pk_bf16_f32 v122, v112, v113
	v_lshlrev_b64 v[112:113], 12, v[138:139]
	v_lshl_add_u64 v[112:113], s[14:15], 0, v[112:113]
	v_lshlrev_b64 v[140:141], 1, v[140:141]
	v_lshl_add_u64 v[112:113], v[112:113], 0, v[140:141]
	v_cvt_pk_bf16_f32 v123, v114, v115
	global_store_dwordx4 v[112:113], v[120:123], off
	v_cvt_pk_bf16_f32 v114, v124, v125
	v_cvt_pk_bf16_f32 v115, v126, v127
	v_cvt_pk_bf16_f32 v116, v116, v117
	v_cvt_pk_bf16_f32 v117, v118, v119
	global_store_dwordx4 v[112:113], v[114:117], off offset:256
	v_cvt_pk_bf16_f32 v100, v100, v101
	v_cvt_pk_bf16_f32 v101, v102, v103
	v_cvt_pk_bf16_f32 v102, v96, v97
	v_cvt_pk_bf16_f32 v103, v98, v99
	s_nop 1
	v_or_b32_e32 v114, 16, v138
	v_ashrrev_i32_e32 v115, 31, v114
	v_lshlrev_b64 v[96:97], 12, v[114:115]
	v_lshl_add_u64 v[96:97], s[14:15], 0, v[96:97]
	v_lshl_add_u64 v[114:115], v[96:97], 0, v[140:141]
	global_store_dwordx4 v[114:115], v[100:103], off
	v_cvt_pk_bf16_f32 v96, v108, v109
	v_cvt_pk_bf16_f32 v97, v110, v111
	v_cvt_pk_bf16_f32 v98, v104, v105
	v_cvt_pk_bf16_f32 v99, v106, v107
	global_store_dwordx4 v[114:115], v[96:99], off offset:256
	v_cvt_pk_bf16_f32 v84, v84, v85
	v_cvt_pk_bf16_f32 v85, v86, v87
	v_cvt_pk_bf16_f32 v86, v80, v81
	v_cvt_pk_bf16_f32 v87, v82, v83
	s_nop 1
	v_or_b32_e32 v96, 32, v138
	v_ashrrev_i32_e32 v97, 31, v96
	v_lshlrev_b64 v[80:81], 12, v[96:97]
	v_lshl_add_u64 v[80:81], s[14:15], 0, v[80:81]
	v_lshl_add_u64 v[96:97], v[80:81], 0, v[140:141]
	global_store_dwordx4 v[96:97], v[84:87], off
	v_cvt_pk_bf16_f32 v80, v92, v93
	v_cvt_pk_bf16_f32 v81, v94, v95
	v_cvt_pk_bf16_f32 v82, v88, v89
	v_cvt_pk_bf16_f32 v83, v90, v91
	global_store_dwordx4 v[96:97], v[80:83], off offset:256
	v_cvt_pk_bf16_f32 v68, v68, v69
	v_cvt_pk_bf16_f32 v69, v70, v71
	v_cvt_pk_bf16_f32 v70, v64, v65
	v_cvt_pk_bf16_f32 v71, v66, v67
	s_nop 1
	v_or_b32_e32 v80, 48, v138
	v_ashrrev_i32_e32 v81, 31, v80
	v_lshlrev_b64 v[64:65], 12, v[80:81]
	v_lshl_add_u64 v[64:65], s[14:15], 0, v[64:65]
	v_lshl_add_u64 v[80:81], v[64:65], 0, v[140:141]
	global_store_dwordx4 v[80:81], v[68:71], off
	v_cvt_pk_bf16_f32 v64, v76, v77
	v_cvt_pk_bf16_f32 v65, v78, v79
	v_cvt_pk_bf16_f32 v66, v72, v73
	v_cvt_pk_bf16_f32 v67, v74, v75
	global_store_dwordx4 v[80:81], v[64:67], off offset:256
	v_cvt_pk_bf16_f32 v56, v56, v57
	v_cvt_pk_bf16_f32 v57, v58, v59
	v_cvt_pk_bf16_f32 v58, v48, v49
	v_add_co_u32_e32 v48, vcc, s36, v112
	s_nop 0
	v_lshl_add_u64 v[64:65], v[112:113], 0, s[18:19]
	v_addc_co_u32_e32 v49, vcc, 0, v113, vcc
	v_cvt_pk_bf16_f32 v59, v50, v51
	global_store_dwordx4 v[48:49], v[56:59], off
	v_cvt_pk_bf16_f32 v48, v60, v61
	v_cvt_pk_bf16_f32 v49, v62, v63
	v_cvt_pk_bf16_f32 v50, v52, v53
	v_cvt_pk_bf16_f32 v51, v54, v55
	global_store_dwordx4 v[64:65], v[48:51], off offset:256
	v_cvt_pk_bf16_f32 v40, v40, v41
	v_cvt_pk_bf16_f32 v41, v42, v43
	v_cvt_pk_bf16_f32 v42, v32, v33
	v_add_co_u32_e32 v32, vcc, s45, v112
	s_nop 0
	v_lshl_add_u64 v[48:49], v[112:113], 0, s[20:21]
	v_addc_co_u32_e32 v33, vcc, 0, v113, vcc
	v_cvt_pk_bf16_f32 v43, v34, v35
	global_store_dwordx4 v[32:33], v[40:43], off
	v_cvt_pk_bf16_f32 v32, v44, v45
	v_cvt_pk_bf16_f32 v33, v46, v47
	v_cvt_pk_bf16_f32 v34, v36, v37
	v_cvt_pk_bf16_f32 v35, v38, v39
	global_store_dwordx4 v[48:49], v[32:35], off offset:256
	v_cvt_pk_bf16_f32 v24, v24, v25
	v_cvt_pk_bf16_f32 v25, v26, v27
	v_cvt_pk_bf16_f32 v26, v16, v17
	v_add_co_u32_e32 v16, vcc, s46, v112
	s_nop 0
	v_lshl_add_u64 v[32:33], v[112:113], 0, s[22:23]
	v_addc_co_u32_e32 v17, vcc, 0, v113, vcc
	v_cvt_pk_bf16_f32 v27, v18, v19
	global_store_dwordx4 v[16:17], v[24:27], off
	v_cvt_pk_bf16_f32 v16, v28, v29
	v_cvt_pk_bf16_f32 v17, v30, v31
	v_cvt_pk_bf16_f32 v18, v20, v21
	v_cvt_pk_bf16_f32 v19, v22, v23
	global_store_dwordx4 v[32:33], v[16:19], off offset:256
	v_cvt_pk_bf16_f32 v4, v4, v5
	v_cvt_pk_bf16_f32 v5, v6, v7
	v_cvt_pk_bf16_f32 v6, v0, v1
	v_add_co_u32_e32 v0, vcc, s47, v112
	v_cvt_pk_bf16_f32 v7, v2, v3
	s_nop 0
	v_lshl_add_u64 v[16:17], v[112:113], 0, s[24:25]
	v_addc_co_u32_e32 v1, vcc, 0, v113, vcc
	global_store_dwordx4 v[0:1], v[4:7], off
	v_cvt_pk_bf16_f32 v0, v8, v9
	v_cvt_pk_bf16_f32 v1, v10, v11
	v_cvt_pk_bf16_f32 v2, v12, v13
	v_cvt_pk_bf16_f32 v3, v14, v15
	s_and_b64 vcc, exec, s[2:3]
	s_mov_b64 s[2:3], -1
	global_store_dwordx4 v[16:17], v[0:3], off offset:256
	s_cbranch_vccnz .LBB0_945
	s_andn2_b64 vcc, exec, s[12:13]
	v_mov_b64 v[120:121], 0
	v_mov_b64 v[122:123], 0
	v_mov_b64 v[112:113], 0
	v_mov_b64 v[114:115], 0
	v_mov_b64 v[100:101], 0
	v_mov_b64 v[102:103], 0
	v_mov_b64 v[96:97], 0
	v_mov_b64 v[98:99], 0
	v_mov_b64 v[84:85], 0
	v_mov_b64 v[86:87], 0
	v_mov_b64 v[80:81], 0
	v_mov_b64 v[82:83], 0
	v_mov_b64 v[68:69], 0
	v_mov_b64 v[70:71], 0
	v_mov_b64 v[64:65], 0
	v_mov_b64 v[66:67], 0
	v_mov_b64 v[124:125], 0
	v_mov_b64 v[126:127], 0
	v_mov_b64 v[116:117], 0
	v_mov_b64 v[118:119], 0
	v_mov_b64 v[108:109], 0
	v_mov_b64 v[110:111], 0
	v_mov_b64 v[104:105], 0
	v_mov_b64 v[106:107], 0
	v_mov_b64 v[92:93], 0
	v_mov_b64 v[94:95], 0
	v_mov_b64 v[88:89], 0
	v_mov_b64 v[90:91], 0
	v_mov_b64 v[76:77], 0
	v_mov_b64 v[78:79], 0
	v_mov_b64 v[72:73], 0
	v_mov_b64 v[74:75], 0
	v_mov_b64 v[56:57], 0
	v_mov_b64 v[58:59], 0
	v_mov_b64 v[48:49], 0
	v_mov_b64 v[50:51], 0
	v_mov_b64 v[40:41], 0
	v_mov_b64 v[42:43], 0
	v_mov_b64 v[32:33], 0
	v_mov_b64 v[34:35], 0
	v_mov_b64 v[24:25], 0
	v_mov_b64 v[26:27], 0
	v_mov_b64 v[16:17], 0
	v_mov_b64 v[18:19], 0
	v_mov_b64 v[4:5], 0
	v_mov_b64 v[6:7], 0
	v_mov_b64 v[0:1], 0
	v_mov_b64 v[2:3], 0
	v_mov_b64 v[60:61], 0
	v_mov_b64 v[62:63], 0
	v_mov_b64 v[52:53], 0
	v_mov_b64 v[54:55], 0
	v_mov_b64 v[44:45], 0
	v_mov_b64 v[46:47], 0
	v_mov_b64 v[36:37], 0
	v_mov_b64 v[38:39], 0
	v_mov_b64 v[28:29], 0
	v_mov_b64 v[30:31], 0
	v_mov_b64 v[20:21], 0
	v_mov_b64 v[22:23], 0
	v_mov_b64 v[8:9], 0
	v_mov_b64 v[10:11], 0
	v_mov_b64 v[12:13], 0
	v_mov_b64 v[14:15], 0
	s_cbranch_vccnz .LBB0_944
	s_barrier
	s_branch .LBB0_944

.LBB0_1147:
	s_add_u32 s4, s92, 0x50ee1c00
	s_addc_u32 s5, s93, 0
	s_add_u32 s8, s92, 0x38ee1c00
	s_addc_u32 s3, s93, 0
	s_add_u32 s12, s92, 0x176e1c00
	s_addc_u32 s13, s93, 0
	s_lshl_b32 s2, s86, 10
	v_lshl_or_b32 v0, v133, 4, s2
	v_ashrrev_i32_e32 v1, 31, v0
	v_lshrrev_b32_e32 v1, 22, v1
	v_add_u32_e32 v1, v0, v1
	v_ashrrev_i32_e32 v132, 10, v1
	v_mul_i32_i24_e32 v1, 0x400, v132
	v_sub_u32_e32 v1, v0, v1
	v_lshrrev_b32_e32 v2, 4, v1
	v_bitop3_b32 v138, v2, v1, 32 bitop3:0x6c
	v_ashrrev_i32_e32 v2, 31, v138
	v_lshrrev_b32_e32 v2, 26, v2
	v_lshlrev_b32_e32 v1, 3, v132
	v_add_u32_e32 v139, v138, v2
	v_and_b32_e32 v1, -16, v1
	v_ashrrev_i32_e32 v140, 6, v139
	v_add_u32_e32 v0, 0x2000, v0
	v_add_u32_e32 v152, v140, v1
	v_ashrrev_i32_e32 v1, 31, v0
	v_lshrrev_b32_e32 v1, 22, v1
	v_add_u32_e32 v1, v0, v1
	v_ashrrev_i32_e32 v141, 10, v1
	v_mul_i32_i24_e32 v1, 0x400, v141
	v_sub_u32_e32 v0, v0, v1
	v_lshrrev_b32_e32 v1, 4, v0
	v_bitop3_b32 v142, v1, v0, 32 bitop3:0x6c
	v_ashrrev_i32_e32 v1, 31, v142
	v_ashrrev_i32_e32 v129, 31, v128
	v_lshrrev_b32_e32 v1, 26, v1
	s_add_i32 s9, s38, -1
	v_lshlrev_b64 v[134:135], 18, v[128:129]
	v_lshlrev_b32_e32 v0, 3, v141
	v_add_u32_e32 v143, v142, v1
	v_min_i32_e32 v130, s9, v152
	v_lshl_add_u64 v[134:135], s[12:13], 0, v[134:135]
	s_lshl_b64 s[6:7], s[6:7], 2
	v_and_b32_e32 v0, -16, v0
	v_ashrrev_i32_e32 v144, 6, v143
	v_ashrrev_i32_e32 v131, 31, v130
	v_lshl_add_u64 v[134:135], v[134:135], 0, s[6:7]
	v_add_u32_e32 v153, v144, v0
	v_lshl_add_u64 v[130:131], v[130:131], 2, v[134:135]
	v_add_u32_e32 v154, 0x80, v152
	v_mov_b64 v[124:125], 0
	v_mov_b64 v[126:127], 0
	v_mov_b64 v[120:121], 0
	v_mov_b64 v[122:123], 0
	v_mov_b64 v[108:109], 0
	v_mov_b64 v[110:111], 0
	v_mov_b64 v[104:105], 0
	v_mov_b64 v[106:107], 0
	v_mov_b64 v[92:93], 0
	v_mov_b64 v[94:95], 0
	v_mov_b64 v[88:89], 0
	v_mov_b64 v[90:91], 0
	v_mov_b64 v[76:77], 0
	v_mov_b64 v[78:79], 0
	v_mov_b64 v[72:73], 0
	v_mov_b64 v[74:75], 0
	v_mov_b64 v[116:117], 0
	v_mov_b64 v[118:119], 0
	v_mov_b64 v[112:113], 0
	v_mov_b64 v[114:115], 0
	v_mov_b64 v[100:101], 0
	v_mov_b64 v[102:103], 0
	v_mov_b64 v[96:97], 0
	v_mov_b64 v[98:99], 0
	v_mov_b64 v[84:85], 0
	v_mov_b64 v[86:87], 0
	v_mov_b64 v[80:81], 0
	v_mov_b64 v[82:83], 0
	v_mov_b64 v[68:69], 0
	v_mov_b64 v[70:71], 0
	v_mov_b64 v[64:65], 0
	v_mov_b64 v[66:67], 0
	s_waitcnt vmcnt(7)
	v_mov_b64 v[60:61], 0
	v_mov_b64 v[62:63], 0
	s_waitcnt vmcnt(4)
	v_mov_b64 v[56:57], 0
	v_mov_b64 v[58:59], 0
	v_mov_b64 v[44:45], 0
	v_mov_b64 v[46:47], 0
	v_mov_b64 v[40:41], 0
	v_mov_b64 v[42:43], 0
	v_mov_b64 v[28:29], 0
	v_mov_b64 v[30:31], 0
	v_mov_b64 v[24:25], 0
	v_mov_b64 v[26:27], 0
	v_mov_b64 v[12:13], 0
	v_mov_b64 v[14:15], 0
	v_mov_b64 v[8:9], 0
	v_mov_b64 v[10:11], 0
	v_mov_b64 v[52:53], 0
	v_mov_b64 v[54:55], 0
	v_mov_b64 v[48:49], 0
	v_mov_b64 v[50:51], 0
	v_mov_b64 v[36:37], 0
	v_mov_b64 v[38:39], 0
	v_mov_b64 v[32:33], 0
	v_mov_b64 v[34:35], 0
	v_mov_b64 v[20:21], 0
	v_mov_b64 v[22:23], 0
	v_mov_b64 v[16:17], 0
	v_mov_b64 v[18:19], 0
	v_mov_b64 v[4:5], 0
	v_mov_b64 v[6:7], 0
	v_mov_b64 v[0:1], 0
	v_mov_b64 v[2:3], 0
	global_load_dword v129, v[130:131], off
	v_min_i32_e32 v130, s9, v153
	v_min_i32_e32 v136, s9, v154
	v_ashrrev_i32_e32 v131, 31, v130
	v_ashrrev_i32_e32 v137, 31, v136
	v_lshl_add_u64 v[130:131], v[130:131], 2, v[134:135]
	v_lshl_add_u64 v[136:137], v[136:137], 2, v[134:135]
	v_add_u32_e32 v155, 0x80, v153
	global_load_dword v145, v[130:131], off
	s_nop 0
	global_load_dword v136, v[136:137], off
	v_min_i32_e32 v130, s9, v155
	v_ashrrev_i32_e32 v131, 31, v130
	v_lshl_add_u64 v[130:131], v[130:131], 2, v[134:135]
	global_load_dword v134, v[130:131], off
	v_and_b32_e32 v131, 0xc0, v139
	v_lshlrev_b32_e32 v130, 5, v132
	v_sub_u32_e32 v131, v138, v131
	v_mov_b32_e32 v132, 1
	v_and_b32_e32 v130, 32, v130
	v_ashrrev_i16_sdwa v131, v132, sext(v131) dst_sel:DWORD dst_unused:UNUSED_PAD src0_sel:DWORD src1_sel:BYTE_0
	v_add_u32_sdwa v156, v130, sext(v131) dst_sel:DWORD dst_unused:UNUSED_PAD src0_sel:DWORD src1_sel:WORD_0
	v_lshlrev_b32_e32 v130, 1, v152
	v_lshrrev_b32_e32 v131, 2, v152
	v_and_b32_e32 v135, 3, v140
	s_mov_b32 s6, 0x1fffe0
	v_and_b32_e32 v130, 24, v130
	v_and_b32_e32 v131, 4, v131
	v_and_or_b32 v135, v152, s6, v135
	v_or3_b32 v130, v135, v131, v130
	v_lshlrev_b32_e32 v131, 1, v156
	v_lshl_add_u32 v157, v130, 11, v131
	v_and_b32_e32 v131, 0xffc0, v143
	v_sub_u32_e32 v131, v142, v131
	v_lshrrev_b16_e32 v135, 7, v131
	v_and_b32_e32 v135, 1, v135
	v_lshlrev_b32_e32 v130, 5, v141
	v_add_u16_e32 v131, v131, v135
	v_and_b32_e32 v130, 32, v130
	v_ashrrev_i16_sdwa v131, v132, sext(v131) dst_sel:DWORD dst_unused:UNUSED_PAD src0_sel:DWORD src1_sel:BYTE_0
	v_add_u32_sdwa v158, v130, sext(v131) dst_sel:DWORD dst_unused:UNUSED_PAD src0_sel:DWORD src1_sel:WORD_0
	v_lshlrev_b32_e32 v130, 1, v153
	v_lshrrev_b32_e32 v131, 2, v153
	v_and_b32_e32 v132, 3, v144
	v_and_b32_e32 v130, 24, v130
	v_and_b32_e32 v131, 4, v131
	v_and_or_b32 v132, v153, s6, v132
	v_or3_b32 v130, v132, v131, v130
	s_and_b32 s9, s3, 0xffff
	s_lshl_b32 s3, s65, 18
	s_add_i32 s25, s2, 0
	s_mov_b32 s7, 0x20000
	s_mov_b32 s6, -1
	s_add_i32 s26, s25, 0x10000
	v_lshlrev_b32_e32 v131, 1, v158
	s_mov_b32 s10, s6
	s_mov_b32 s11, s7
	s_mov_b32 m0, s26
	s_add_i32 s27, s25, 0x12000
	v_lshl_add_u32 v159, v130, 11, v131
	s_add_i32 s28, s25, 0x14000
	s_add_i32 s29, s25, 0x16000
	s_and_b32 s5, s5, 0xffff
	s_add_i32 s30, s25, 0x2000
	s_add_i32 s31, s25, 0x4000
	s_add_i32 s33, s25, 0x6000
	s_mov_b32 s34, 0
	s_waitcnt vmcnt(3)
	v_lshlrev_b32_e32 v129, 8, v129
	v_and_b32_e32 v129, 0x7ffffc00, v129
	v_add_lshl_u32 v129, v129, v156, 1
	s_waitcnt vmcnt(2)
	v_lshlrev_b32_e32 v130, 8, v145
	v_and_b32_e32 v130, 0x7ffffc00, v130
	s_waitcnt vmcnt(1)
	v_lshlrev_b32_e32 v131, 8, v136
	v_add_lshl_u32 v130, v130, v158, 1
	v_and_b32_e32 v131, 0x7ffffc00, v131
	s_waitcnt vmcnt(0)
	v_lshlrev_b32_e32 v132, 8, v134
	v_lshlrev_b32_e32 v134, 22, v128
	v_add_u32_e32 v134, s3, v134
	v_add_lshl_u32 v131, v131, v156, 1
	v_readfirstlane_b32 s3, v134
	s_lshl_b32 s66, s3, 1
	buffer_load_dwordx4 v157, s[8:11], s66 offen lds
	s_mov_b32 m0, s27
	s_add_i32 s2, s66, 0x40000
	buffer_load_dwordx4 v159, s[8:11], s66 offen lds
	s_mov_b32 m0, s28
	v_and_b32_e32 v132, 0x7ffffc00, v132
	buffer_load_dwordx4 v157, s[8:11], s2 offen lds
	s_mov_b32 m0, s29
	v_add_lshl_u32 v132, v132, v158, 1
	buffer_load_dwordx4 v159, s[8:11], s2 offen lds
	s_mov_b32 m0, s25
	s_lshr_b32 s2, s90, 8
	buffer_load_dwordx4 v129, s[4:7], 0 offen lds
	s_mov_b32 m0, s30
	s_cmp_eq_u32 s2, 1
	buffer_load_dwordx4 v130, s[4:7], 0 offen lds
	s_mov_b32 m0, s31
	s_movk_i32 s3, 0x80
	buffer_load_dwordx4 v131, s[4:7], 0 offen lds
	s_mov_b32 m0, s33
	s_cselect_b64 s[14:15], -1, 0
	buffer_load_dwordx4 v132, s[4:7], 0 offen lds
	s_cmp_lg_u32 s2, 1
	s_cbranch_scc1 .LBB0_1149
	s_barrier

.LBB0_1176:
	s_or_b64 exec, exec, s[10:11]
	s_and_b64 vcc, exec, s[2:3]
	s_mov_b64 s[2:3], -1
	s_cbranch_vccnz .LBB0_1151
	s_andn2_b64 vcc, exec, s[14:15]
	v_mov_b64 v[124:125], 0
	v_mov_b64 v[126:127], 0
	v_mov_b64 v[120:121], 0
	v_mov_b64 v[122:123], 0
	v_mov_b64 v[108:109], 0
	v_mov_b64 v[110:111], 0
	v_mov_b64 v[104:105], 0
	v_mov_b64 v[106:107], 0
	v_mov_b64 v[92:93], 0
	v_mov_b64 v[94:95], 0
	v_mov_b64 v[88:89], 0
	v_mov_b64 v[90:91], 0
	v_mov_b64 v[76:77], 0
	v_mov_b64 v[78:79], 0
	v_mov_b64 v[72:73], 0
	v_mov_b64 v[74:75], 0
	v_mov_b64 v[116:117], 0
	v_mov_b64 v[118:119], 0
	v_mov_b64 v[112:113], 0
	v_mov_b64 v[114:115], 0
	v_mov_b64 v[100:101], 0
	v_mov_b64 v[102:103], 0
	v_mov_b64 v[96:97], 0
	v_mov_b64 v[98:99], 0
	v_mov_b64 v[84:85], 0
	v_mov_b64 v[86:87], 0
	v_mov_b64 v[80:81], 0
	v_mov_b64 v[82:83], 0
	v_mov_b64 v[68:69], 0
	v_mov_b64 v[70:71], 0
	v_mov_b64 v[64:65], 0
	v_mov_b64 v[66:67], 0
	v_mov_b64 v[60:61], 0
	v_mov_b64 v[62:63], 0
	v_mov_b64 v[56:57], 0
	v_mov_b64 v[58:59], 0
	v_mov_b64 v[44:45], 0
	v_mov_b64 v[46:47], 0
	v_mov_b64 v[40:41], 0
	v_mov_b64 v[42:43], 0
	v_mov_b64 v[28:29], 0
	v_mov_b64 v[30:31], 0
	v_mov_b64 v[24:25], 0
	v_mov_b64 v[26:27], 0
	v_mov_b64 v[12:13], 0
	v_mov_b64 v[14:15], 0
	v_mov_b64 v[8:9], 0
	v_mov_b64 v[10:11], 0
	v_mov_b64 v[52:53], 0
	v_mov_b64 v[54:55], 0
	v_mov_b64 v[48:49], 0
	v_mov_b64 v[50:51], 0
	v_mov_b64 v[36:37], 0
	v_mov_b64 v[38:39], 0
	v_mov_b64 v[32:33], 0
	v_mov_b64 v[34:35], 0
	v_mov_b64 v[20:21], 0
	v_mov_b64 v[22:23], 0
	v_mov_b64 v[16:17], 0
	v_mov_b64 v[18:19], 0
	v_mov_b64 v[4:5], 0
	v_mov_b64 v[6:7], 0
	v_mov_b64 v[0:1], 0
	v_mov_b64 v[2:3], 0
	s_cbranch_vccnz .LBB0_1150
	s_barrier
	s_branch .LBB0_1150

.LBB0_1243:
	s_andn2_b64 vcc, exec, s[2:3]
	s_cbranch_vccnz .LBB0_1277
	s_add_u32 s20, s92, 0x52ee1c00
	s_addc_u32 s2, s93, 0
	s_add_u32 s24, s92, 0x48ee1c00
	s_addc_u32 s3, s93, 0
	s_lshl_b32 s5, s86, 10
	v_lshl_or_b32 v0, v132, 4, s5
	v_ashrrev_i32_e32 v1, 31, v0
	v_lshrrev_b32_e32 v1, 22, v1
	v_add_u32_e32 v1, v0, v1
	v_ashrrev_i32_e32 v1, 10, v1
	v_mul_i32_i24_e32 v2, 0x400, v1
	v_sub_u32_e32 v2, v0, v2
	v_lshrrev_b32_e32 v3, 4, v2
	v_bitop3_b32 v2, v3, v2, 32 bitop3:0x6c
	s_waitcnt vmcnt(8)
	v_ashrrev_i32_e32 v4, 31, v2
	v_lshrrev_b32_e32 v4, 26, v4
	v_lshlrev_b32_e32 v3, 3, v1
	v_add_u32_e32 v4, v2, v4
	v_and_b32_e32 v3, -16, v3
	v_ashrrev_i32_e32 v5, 6, v4
	v_add_u32_e32 v151, v5, v3
	v_and_b32_e32 v3, 0xc0, v4
	v_sub_u32_e32 v2, v2, v3
	v_mov_b32_e32 v3, 1
	v_lshlrev_b32_e32 v1, 5, v1
	v_ashrrev_i16_sdwa v2, v3, sext(v2) dst_sel:DWORD dst_unused:UNUSED_PAD src0_sel:DWORD src1_sel:BYTE_0
	v_and_b32_e32 v1, 32, v1
	v_bfe_i32 v2, v2, 0, 16
	v_add_u32_e32 v0, 0x2000, v0
	v_add_lshl_u32 v153, v1, v2, 1
	v_ashrrev_i32_e32 v1, 31, v0
	v_lshrrev_b32_e32 v1, 22, v1
	v_add_u32_e32 v1, v0, v1
	v_ashrrev_i32_e32 v1, 10, v1
	v_mul_i32_i24_e32 v2, 0x400, v1
	v_lshlrev_b32_e32 v4, 1, v151
	v_lshrrev_b32_e32 v6, 2, v151
	v_and_b32_e32 v5, 3, v5
	s_mov_b32 s6, 0x1fffe0
	v_sub_u32_e32 v0, v0, v2
	v_and_b32_e32 v4, 24, v4
	v_and_b32_e32 v6, 4, v6
	v_and_or_b32 v5, v151, s6, v5
	v_lshrrev_b32_e32 v2, 4, v0
	v_or3_b32 v4, v5, v6, v4
	v_bitop3_b32 v0, v2, v0, 32 bitop3:0x6c
	v_lshl_add_u32 v155, v4, 11, v153
	v_ashrrev_i32_e32 v4, 31, v0
	v_lshrrev_b32_e32 v4, 26, v4
	v_lshlrev_b32_e32 v2, 3, v1
	v_add_u32_e32 v4, v0, v4
	v_and_b32_e32 v2, -16, v2
	v_ashrrev_i32_e32 v5, 6, v4
	v_add_u32_e32 v157, v5, v2
	v_and_b32_e32 v2, 0xffc0, v4
	v_sub_u32_e32 v0, v0, v2
	v_lshrrev_b16_e32 v2, 7, v0
	v_and_b32_e32 v2, 1, v2
	s_and_b32 s21, s2, 0xffff
	s_add_i32 s2, s81, -1
	v_add_u32_e32 v166, 0x80, v151
	v_add_u32_e32 v167, 0x80, v157
	v_add_u16_e32 v0, v0, v2
	v_min_i32_e32 v128, s2, v151
	v_min_i32_e32 v129, s2, v157
	v_min_i32_e32 v130, s2, v166
	v_min_i32_e32 v131, s2, v167
	v_lshlrev_b32_e32 v133, 21, v146
	s_lshl_b32 s2, s1, 18
	v_lshlrev_b32_e32 v1, 5, v1
	v_ashrrev_i16_sdwa v0, v3, sext(v0) dst_sel:DWORD dst_unused:UNUSED_PAD src0_sel:DWORD src1_sel:BYTE_0
	v_lshlrev_b32_e32 v2, 1, v157
	v_lshrrev_b32_e32 v3, 2, v157
	v_and_b32_e32 v4, 3, v5
	v_add_u32_e32 v133, s2, v133
	s_add_i32 s42, s5, 0
	v_and_b32_e32 v1, 32, v1
	v_bfe_i32 v0, v0, 0, 16
	v_and_b32_e32 v2, 24, v2
	v_and_b32_e32 v3, 4, v3
	v_and_or_b32 v4, v157, s6, v4
	s_mov_b32 s23, 0x20000
	s_mov_b32 s22, -1
	v_readfirstlane_b32 s2, v133
	s_add_i32 s43, s42, 0x10000
	v_or3_b32 v2, v4, v3, v2
	v_add_lshl_u32 v159, v1, v0, 1
	s_and_b32 s25, s3, 0xffff
	s_mov_b32 s26, s22
	s_mov_b32 s27, s23
	s_lshl_b32 s6, s2, 1
	s_mov_b32 m0, s43
	s_add_i32 s44, s42, 0x12000
	v_lshl_add_u32 v161, v2, 11, v159
	v_mov_b64 v[124:125], 0
	v_mov_b64 v[126:127], 0
	v_mov_b64 v[120:121], 0
	v_mov_b64 v[122:123], 0
	v_mov_b64 v[108:109], 0
	v_mov_b64 v[110:111], 0
	v_mov_b64 v[104:105], 0
	v_mov_b64 v[106:107], 0
	v_mov_b64 v[92:93], 0
	v_mov_b64 v[94:95], 0
	v_mov_b64 v[88:89], 0
	v_mov_b64 v[90:91], 0
	v_mov_b64 v[76:77], 0
	v_mov_b64 v[78:79], 0
	v_mov_b64 v[72:73], 0
	v_mov_b64 v[74:75], 0
	v_mov_b64 v[116:117], 0
	v_mov_b64 v[118:119], 0
	v_mov_b64 v[112:113], 0
	v_mov_b64 v[114:115], 0
	v_mov_b64 v[100:101], 0
	v_mov_b64 v[102:103], 0
	v_mov_b64 v[96:97], 0
	v_mov_b64 v[98:99], 0
	v_mov_b64 v[84:85], 0
	v_mov_b64 v[86:87], 0
	v_mov_b64 v[80:81], 0
	v_mov_b64 v[82:83], 0
	v_mov_b64 v[68:69], 0
	v_mov_b64 v[70:71], 0
	v_mov_b64 v[64:65], 0
	v_mov_b64 v[66:67], 0
	s_waitcnt vmcnt(7)
	v_mov_b64 v[60:61], 0
	v_mov_b64 v[62:63], 0
	s_waitcnt vmcnt(4)
	v_mov_b64 v[56:57], 0
	v_mov_b64 v[58:59], 0
	v_mov_b64 v[44:45], 0
	v_mov_b64 v[46:47], 0
	v_mov_b64 v[40:41], 0
	v_mov_b64 v[42:43], 0
	v_mov_b64 v[28:29], 0
	v_mov_b64 v[30:31], 0
	v_mov_b64 v[24:25], 0
	v_mov_b64 v[26:27], 0
	v_mov_b64 v[12:13], 0
	v_mov_b64 v[14:15], 0
	v_mov_b64 v[8:9], 0
	v_mov_b64 v[10:11], 0
	v_mov_b64 v[52:53], 0
	v_mov_b64 v[54:55], 0
	v_mov_b64 v[48:49], 0
	v_mov_b64 v[50:51], 0
	v_mov_b64 v[36:37], 0
	v_mov_b64 v[38:39], 0
	v_mov_b64 v[32:33], 0
	v_mov_b64 v[34:35], 0
	v_mov_b64 v[20:21], 0
	v_mov_b64 v[22:23], 0
	v_mov_b64 v[16:17], 0
	v_mov_b64 v[18:19], 0
	v_mov_b64 v[4:5], 0
	v_mov_b64 v[6:7], 0
	v_mov_b64 v[0:1], 0
	v_mov_b64 v[2:3], 0
	buffer_load_dwordx4 v155, s[24:27], s6 offen lds
	s_mov_b32 m0, s44
	s_add_i32 s45, s42, 0x14000
	buffer_load_dwordx4 v161, s[24:27], s6 offen lds
	s_add_i32 s2, s6, 0x40000
	s_mov_b32 m0, s45
	s_add_i32 s46, s42, 0x16000
	v_add_u32_e32 v128, s4, v128
	buffer_load_dwordx4 v155, s[24:27], s2 offen lds
	s_mov_b32 m0, s46
	v_lshl_add_u32 v128, v128, 11, v153
	v_add_u32_e32 v129, s4, v129
	buffer_load_dwordx4 v161, s[24:27], s2 offen lds
	s_mov_b32 m0, s42
	s_add_i32 s47, s42, 0x2000
	v_lshl_add_u32 v129, v129, 11, v159
	v_add_u32_e32 v130, s4, v130
	buffer_load_dwordx4 v128, s[20:23], 0 offen lds
	s_mov_b32 m0, s47
	s_add_i32 s48, s42, 0x4000
	v_lshl_add_u32 v130, v130, 11, v153
	v_add_u32_e32 v131, s4, v131
	buffer_load_dwordx4 v129, s[20:23], 0 offen lds
	s_mov_b32 m0, s48
	s_add_i32 s49, s42, 0x6000
	v_lshl_add_u32 v131, v131, 11, v159
	buffer_load_dwordx4 v130, s[20:23], 0 offen lds
	s_mov_b32 m0, s49
	s_lshr_b32 s2, s90, 8
	buffer_load_dwordx4 v131, s[20:23], 0 offen lds
	s_cmp_eq_u32 s2, 1
	s_movk_i32 s3, 0x80
	s_cselect_b64 s[28:29], -1, 0
	s_cmp_lg_u32 s2, 1
	s_mov_b32 s50, 0
	s_cbranch_scc1 .LBB0_1246
	s_barrier

.LBB0_1273:
	s_or_b64 exec, exec, s[0:1]
	s_and_b64 vcc, exec, s[2:3]
	s_mov_b64 s[0:1], -1
	s_cbranch_vccnz .LBB0_1248
	s_andn2_b64 vcc, exec, s[28:29]
	v_mov_b64 v[124:125], 0
	v_mov_b64 v[126:127], 0
	v_mov_b64 v[120:121], 0
	v_mov_b64 v[122:123], 0
	v_mov_b64 v[108:109], 0
	v_mov_b64 v[110:111], 0
	v_mov_b64 v[104:105], 0
	v_mov_b64 v[106:107], 0
	v_mov_b64 v[92:93], 0
	v_mov_b64 v[94:95], 0
	v_mov_b64 v[88:89], 0
	v_mov_b64 v[90:91], 0
	v_mov_b64 v[76:77], 0
	v_mov_b64 v[78:79], 0
	v_mov_b64 v[72:73], 0
	v_mov_b64 v[74:75], 0
	v_mov_b64 v[116:117], 0
	v_mov_b64 v[118:119], 0
	v_mov_b64 v[112:113], 0
	v_mov_b64 v[114:115], 0
	v_mov_b64 v[100:101], 0
	v_mov_b64 v[102:103], 0
	v_mov_b64 v[96:97], 0
	v_mov_b64 v[98:99], 0
	v_mov_b64 v[84:85], 0
	v_mov_b64 v[86:87], 0
	v_mov_b64 v[80:81], 0
	v_mov_b64 v[82:83], 0
	v_mov_b64 v[68:69], 0
	v_mov_b64 v[70:71], 0
	v_mov_b64 v[64:65], 0
	v_mov_b64 v[66:67], 0
	v_mov_b64 v[60:61], 0
	v_mov_b64 v[62:63], 0
	v_mov_b64 v[56:57], 0
	v_mov_b64 v[58:59], 0
	v_mov_b64 v[44:45], 0
	v_mov_b64 v[46:47], 0
	v_mov_b64 v[40:41], 0
	v_mov_b64 v[42:43], 0
	v_mov_b64 v[28:29], 0
	v_mov_b64 v[30:31], 0
	v_mov_b64 v[24:25], 0
	v_mov_b64 v[26:27], 0
	v_mov_b64 v[12:13], 0
	v_mov_b64 v[14:15], 0
	v_mov_b64 v[8:9], 0
	v_mov_b64 v[10:11], 0
	v_mov_b64 v[52:53], 0
	v_mov_b64 v[54:55], 0
	v_mov_b64 v[48:49], 0
	v_mov_b64 v[50:51], 0
	v_mov_b64 v[36:37], 0
	v_mov_b64 v[38:39], 0
	v_mov_b64 v[32:33], 0
	v_mov_b64 v[34:35], 0
	v_mov_b64 v[20:21], 0
	v_mov_b64 v[22:23], 0
	v_mov_b64 v[16:17], 0
	v_mov_b64 v[18:19], 0
	v_mov_b64 v[4:5], 0
	v_mov_b64 v[6:7], 0
	v_mov_b64 v[0:1], 0
	v_mov_b64 v[2:3], 0
	s_cbranch_vccnz .LBB0_1247
	s_barrier
	s_branch .LBB0_1247
